# MLP1: GELU epilogue of units 0,1 deferred into next unit K-loop (2 VALU per MFMA gap), z parked in v176-239
# baseline (speedup 1.0000x reference)
_Z9k_gemm128IN4g1289EpiGeluLNEEvNS0_4GemmET_:
	s_mov_b32 s78, 0
	s_mov_b32 s79, 0xbf3a00e3
	s_mov_b32 s80, 0x3e6d3388
	s_mov_b32 s82, 0x3f07dc22
	s_mov_b32 s84, 0x3f35f0e3
	s_mov_b32 s86, 0xbe11a98e
	s_mov_b32 s88, 0x3e027906
	s_mov_b32 s90, 0xbf38aa3b
	s_mov_b64 s[92:93], 0x18000
	s_mov_b64 s[94:95], 0x30000
	s_mov_b64 s[96:97], 0x48000
	s_load_dword s3, s[0:1], 0x58
	s_load_dwordx4 s[16:19], s[0:1], 0x10
	s_load_dwordx2 s[20:21], s[0:1], 0x48
	s_load_dwordx8 s[8:15], s[0:1], 0x28
	s_ashr_i32 s35, s2, 31
	s_waitcnt lgkmcnt(0)
	s_ashr_i32 s31, s3, 31
	s_ashr_i32 s4, s16, 31
	s_lshr_b32 s4, s4, 25
	s_add_i32 s4, s16, s4
	s_ashr_i32 s33, s4, 7
	s_ashr_i32 s4, s17, 31
	s_lshr_b32 s4, s4, 24
	s_add_i32 s4, s17, s4
	s_ashr_i32 s4, s4, 8
	s_mul_i32 s26, s4, s33
	s_ashr_i32 s27, s26, 31
	s_lshr_b32 s5, s27, 29
	s_add_i32 s5, s26, s5
	s_ashr_i32 s37, s5, 3
	s_and_b32 s5, s5, -8
	s_sub_i32 s39, s26, s5
	s_add_i32 s50, s37, 1
	s_lshl_b32 s51, s4, 3
	s_cmp_lt_i32 s2, s26
	s_cselect_b64 s[16:17], -1, 0
	s_cmp_ge_i32 s2, s26
	s_mul_i32 s52, s50, s39
	s_cbranch_scc1 .LBB5_34
	s_ashr_i32 s4, s2, 31
	s_lshr_b32 s4, s4, 29
	s_add_i32 s6, s2, s4
	s_and_b32 s4, s6, -8
	s_sub_i32 s7, s2, s4
	s_cmp_ge_i32 s7, s39
	s_cbranch_scc0 .LBB5_3
	s_sub_i32 s4, s7, s39
	s_mul_i32 s4, s4, s37
	s_add_i32 s22, s4, s52
	s_cbranch_execz .LBB5_4
	s_branch .LBB5_5

.LBB5_42:
	s_and_b64 vcc, exec, s[0:1]
	s_cbranch_vccnz .Lg_orig_epi
	s_mul_i32 s40, s74, 0xc00
	s_add_i32 s40, s40, 0
	v_lshl_add_u32 v135, s73, 7, v111
	s_add_i32 s44, s40, 0x24000
	s_waitcnt lgkmcnt(0)
	v_mad_i64_i32 v[96:97], s[42:43], v135, s63, 0
	v_lshl_add_u64 v[126:127], v[96:97], 1, s[8:9]
	v_add_u32_e32 v96, s44, v129
	v_lshl_add_u32 v32, v110, 2, s44
	v_add_u32_e32 v136, 0x800, v96
	ds_read_b128 v[68:71], v32
	ds_read_b128 v[60:63], v32 offset:16
	ds_read_b128 v[64:67], v32 offset:1024
	ds_read_b128 v[56:59], v32 offset:1040
	ds_read_b128 v[44:47], v32 offset:512
	ds_read_b128 v[36:39], v32 offset:528
	ds_read_b128 v[40:43], v32 offset:1536
	ds_read_b128 v[32:35], v32 offset:1552
	ds_read2_b64 v[96:99], v136 offset1:16
	ds_read2_b64 v[240:243], v136 offset0:32 offset1:48
	s_lshl_b32 s40, s72, 8
	s_ashr_i32 s41, s40, 31
	s_lshl_b64 s[40:41], s[40:41], 1
	v_lshl_add_u64 v[126:127], v[126:127], 0, s[40:41]
	v_lshlrev_b32_e32 v108, 1, v110
	v_lshl_add_u64 v[250:251], v[126:127], 0, v[108:109]
	s_waitcnt lgkmcnt(0)
	v_pk_fma_f32 v[176:177], v[68:69], v[96:97], v[92:93] op_sel_hi:[1,0,1] neg_lo:[1,0,0] neg_hi:[1,0,0]
	v_pk_fma_f32 v[178:179], v[70:71], v[96:97], v[94:95] op_sel_hi:[1,0,1] neg_lo:[1,0,0] neg_hi:[1,0,0]
	v_pk_fma_f32 v[180:181], v[60:61], v[96:97], v[88:89] op_sel_hi:[1,0,1] neg_lo:[1,0,0] neg_hi:[1,0,0]
	v_pk_fma_f32 v[182:183], v[62:63], v[96:97], v[90:91] op_sel_hi:[1,0,1] neg_lo:[1,0,0] neg_hi:[1,0,0]
	v_pk_fma_f32 v[176:177], v[96:97], v[176:177], v[64:65] op_sel:[1,0,0]
	v_pk_fma_f32 v[178:179], v[96:97], v[178:179], v[66:67] op_sel:[1,0,0]
	v_pk_fma_f32 v[180:181], v[96:97], v[180:181], v[56:57] op_sel:[1,0,0]
	v_pk_fma_f32 v[182:183], v[96:97], v[182:183], v[58:59] op_sel:[1,0,0]
	v_pk_fma_f32 v[184:185], v[44:45], v[96:97], v[84:85] op_sel_hi:[1,0,1] neg_lo:[1,0,0] neg_hi:[1,0,0]
	v_pk_fma_f32 v[186:187], v[46:47], v[96:97], v[86:87] op_sel_hi:[1,0,1] neg_lo:[1,0,0] neg_hi:[1,0,0]
	v_pk_fma_f32 v[188:189], v[36:37], v[96:97], v[80:81] op_sel_hi:[1,0,1] neg_lo:[1,0,0] neg_hi:[1,0,0]
	v_pk_fma_f32 v[190:191], v[38:39], v[96:97], v[82:83] op_sel_hi:[1,0,1] neg_lo:[1,0,0] neg_hi:[1,0,0]
	v_pk_fma_f32 v[184:185], v[96:97], v[184:185], v[40:41] op_sel:[1,0,0]
	v_pk_fma_f32 v[186:187], v[96:97], v[186:187], v[42:43] op_sel:[1,0,0]
	v_pk_fma_f32 v[188:189], v[96:97], v[188:189], v[32:33] op_sel:[1,0,0]
	v_pk_fma_f32 v[190:191], v[96:97], v[190:191], v[34:35] op_sel:[1,0,0]
	v_pk_fma_f32 v[192:193], v[68:69], v[98:99], v[76:77] op_sel_hi:[1,0,1] neg_lo:[1,0,0] neg_hi:[1,0,0]
	v_pk_fma_f32 v[194:195], v[70:71], v[98:99], v[78:79] op_sel_hi:[1,0,1] neg_lo:[1,0,0] neg_hi:[1,0,0]
	v_pk_fma_f32 v[196:197], v[60:61], v[98:99], v[72:73] op_sel_hi:[1,0,1] neg_lo:[1,0,0] neg_hi:[1,0,0]
	v_pk_fma_f32 v[198:199], v[62:63], v[98:99], v[74:75] op_sel_hi:[1,0,1] neg_lo:[1,0,0] neg_hi:[1,0,0]
	v_pk_fma_f32 v[192:193], v[98:99], v[192:193], v[64:65] op_sel:[1,0,0]
	v_pk_fma_f32 v[194:195], v[98:99], v[194:195], v[66:67] op_sel:[1,0,0]
	v_pk_fma_f32 v[196:197], v[98:99], v[196:197], v[56:57] op_sel:[1,0,0]
	v_pk_fma_f32 v[198:199], v[98:99], v[198:199], v[58:59] op_sel:[1,0,0]
	v_pk_fma_f32 v[200:201], v[44:45], v[98:99], v[52:53] op_sel_hi:[1,0,1] neg_lo:[1,0,0] neg_hi:[1,0,0]
	v_pk_fma_f32 v[202:203], v[46:47], v[98:99], v[54:55] op_sel_hi:[1,0,1] neg_lo:[1,0,0] neg_hi:[1,0,0]
	v_pk_fma_f32 v[204:205], v[36:37], v[98:99], v[48:49] op_sel_hi:[1,0,1] neg_lo:[1,0,0] neg_hi:[1,0,0]
	v_pk_fma_f32 v[206:207], v[38:39], v[98:99], v[50:51] op_sel_hi:[1,0,1] neg_lo:[1,0,0] neg_hi:[1,0,0]
	v_pk_fma_f32 v[200:201], v[98:99], v[200:201], v[40:41] op_sel:[1,0,0]
	v_pk_fma_f32 v[202:203], v[98:99], v[202:203], v[42:43] op_sel:[1,0,0]
	v_pk_fma_f32 v[204:205], v[98:99], v[204:205], v[32:33] op_sel:[1,0,0]
	v_pk_fma_f32 v[206:207], v[98:99], v[206:207], v[34:35] op_sel:[1,0,0]
	v_pk_fma_f32 v[208:209], v[68:69], v[240:241], v[28:29] op_sel_hi:[1,0,1] neg_lo:[1,0,0] neg_hi:[1,0,0]
	v_pk_fma_f32 v[210:211], v[70:71], v[240:241], v[30:31] op_sel_hi:[1,0,1] neg_lo:[1,0,0] neg_hi:[1,0,0]
	v_pk_fma_f32 v[212:213], v[60:61], v[240:241], v[24:25] op_sel_hi:[1,0,1] neg_lo:[1,0,0] neg_hi:[1,0,0]
	v_pk_fma_f32 v[214:215], v[62:63], v[240:241], v[26:27] op_sel_hi:[1,0,1] neg_lo:[1,0,0] neg_hi:[1,0,0]
	v_pk_fma_f32 v[208:209], v[240:241], v[208:209], v[64:65] op_sel:[1,0,0]
	v_pk_fma_f32 v[210:211], v[240:241], v[210:211], v[66:67] op_sel:[1,0,0]
	v_pk_fma_f32 v[212:213], v[240:241], v[212:213], v[56:57] op_sel:[1,0,0]
	v_pk_fma_f32 v[214:215], v[240:241], v[214:215], v[58:59] op_sel:[1,0,0]
	v_pk_fma_f32 v[216:217], v[44:45], v[240:241], v[20:21] op_sel_hi:[1,0,1] neg_lo:[1,0,0] neg_hi:[1,0,0]
	v_pk_fma_f32 v[218:219], v[46:47], v[240:241], v[22:23] op_sel_hi:[1,0,1] neg_lo:[1,0,0] neg_hi:[1,0,0]
	v_pk_fma_f32 v[220:221], v[36:37], v[240:241], v[16:17] op_sel_hi:[1,0,1] neg_lo:[1,0,0] neg_hi:[1,0,0]
	v_pk_fma_f32 v[222:223], v[38:39], v[240:241], v[18:19] op_sel_hi:[1,0,1] neg_lo:[1,0,0] neg_hi:[1,0,0]
	v_pk_fma_f32 v[216:217], v[240:241], v[216:217], v[40:41] op_sel:[1,0,0]
	v_pk_fma_f32 v[218:219], v[240:241], v[218:219], v[42:43] op_sel:[1,0,0]
	v_pk_fma_f32 v[220:221], v[240:241], v[220:221], v[32:33] op_sel:[1,0,0]
	v_pk_fma_f32 v[222:223], v[240:241], v[222:223], v[34:35] op_sel:[1,0,0]
	v_pk_fma_f32 v[224:225], v[68:69], v[242:243], v[12:13] op_sel_hi:[1,0,1] neg_lo:[1,0,0] neg_hi:[1,0,0]
	v_pk_fma_f32 v[226:227], v[70:71], v[242:243], v[14:15] op_sel_hi:[1,0,1] neg_lo:[1,0,0] neg_hi:[1,0,0]
	v_pk_fma_f32 v[228:229], v[60:61], v[242:243], v[8:9] op_sel_hi:[1,0,1] neg_lo:[1,0,0] neg_hi:[1,0,0]
	v_pk_fma_f32 v[230:231], v[62:63], v[242:243], v[10:11] op_sel_hi:[1,0,1] neg_lo:[1,0,0] neg_hi:[1,0,0]
	v_pk_fma_f32 v[224:225], v[242:243], v[224:225], v[64:65] op_sel:[1,0,0]
	v_pk_fma_f32 v[226:227], v[242:243], v[226:227], v[66:67] op_sel:[1,0,0]
	v_pk_fma_f32 v[228:229], v[242:243], v[228:229], v[56:57] op_sel:[1,0,0]
	v_pk_fma_f32 v[230:231], v[242:243], v[230:231], v[58:59] op_sel:[1,0,0]
	v_pk_fma_f32 v[232:233], v[44:45], v[242:243], v[4:5] op_sel_hi:[1,0,1] neg_lo:[1,0,0] neg_hi:[1,0,0]
	v_pk_fma_f32 v[234:235], v[46:47], v[242:243], v[6:7] op_sel_hi:[1,0,1] neg_lo:[1,0,0] neg_hi:[1,0,0]
	v_pk_fma_f32 v[236:237], v[36:37], v[242:243], v[0:1] op_sel_hi:[1,0,1] neg_lo:[1,0,0] neg_hi:[1,0,0]
	v_pk_fma_f32 v[238:239], v[38:39], v[242:243], v[2:3] op_sel_hi:[1,0,1] neg_lo:[1,0,0] neg_hi:[1,0,0]
	v_pk_fma_f32 v[232:233], v[242:243], v[232:233], v[40:41] op_sel:[1,0,0]
	v_pk_fma_f32 v[234:235], v[242:243], v[234:235], v[42:43] op_sel:[1,0,0]
	v_pk_fma_f32 v[236:237], v[242:243], v[236:237], v[32:33] op_sel:[1,0,0]
	v_pk_fma_f32 v[238:239], v[242:243], v[238:239], v[34:35] op_sel:[1,0,0]
	v_mov_b32_e32 v248, s79
	v_mov_b32_e32 v249, s79
	s_mov_b32 s72, s70
	s_mov_b32 s73, s71
	s_mov_b32 s74, s69
	s_mov_b64 s[42:43], s[4:5]
	s_mov_b64 s[40:41], s[6:7]
	s_mov_b32 s78, 1
	s_branch .LBB5_43

.LBB5_53:
	v_mov_b32_e32 v95, 0
	s_andn2_b64 vcc, exec, s[24:25]
	v_mov_b32_e32 v94, v95
	v_mov_b32_e32 v93, v95
	v_mov_b32_e32 v92, v95
	v_mov_b32_e32 v91, v95
	v_mov_b32_e32 v90, v95
	v_mov_b32_e32 v89, v95
	v_mov_b32_e32 v88, v95
	v_mov_b32_e32 v79, v95
	v_mov_b32_e32 v78, v95
	v_mov_b32_e32 v77, v95
	v_mov_b32_e32 v76, v95
	v_mov_b32_e32 v75, v95
	v_mov_b32_e32 v74, v95
	v_mov_b32_e32 v73, v95
	v_mov_b32_e32 v72, v95
	v_mov_b32_e32 v31, v95
	v_mov_b32_e32 v30, v95
	v_mov_b32_e32 v29, v95
	v_mov_b32_e32 v28, v95
	v_mov_b32_e32 v27, v95
	v_mov_b32_e32 v26, v95
	v_mov_b32_e32 v25, v95
	v_mov_b32_e32 v24, v95
	v_mov_b32_e32 v15, v95
	v_mov_b32_e32 v14, v95
	v_mov_b32_e32 v13, v95
	v_mov_b32_e32 v12, v95
	v_mov_b32_e32 v11, v95
	v_mov_b32_e32 v10, v95
	v_mov_b32_e32 v9, v95
	v_mov_b32_e32 v8, v95
	v_mov_b32_e32 v87, v95
	v_mov_b32_e32 v86, v95
	v_mov_b32_e32 v85, v95
	v_mov_b32_e32 v84, v95
	v_mov_b32_e32 v83, v95
	v_mov_b32_e32 v82, v95
	v_mov_b32_e32 v81, v95
	v_mov_b32_e32 v80, v95
	v_mov_b32_e32 v55, v95
	v_mov_b32_e32 v54, v95
	v_mov_b32_e32 v53, v95
	v_mov_b32_e32 v52, v95
	v_mov_b32_e32 v51, v95
	v_mov_b32_e32 v50, v95
	v_mov_b32_e32 v49, v95
	v_mov_b32_e32 v48, v95
	v_mov_b32_e32 v23, v95
	v_mov_b32_e32 v22, v95
	v_mov_b32_e32 v21, v95
	v_mov_b32_e32 v20, v95
	v_mov_b32_e32 v19, v95
	v_mov_b32_e32 v18, v95
	v_mov_b32_e32 v17, v95
	v_mov_b32_e32 v16, v95
	v_mov_b32_e32 v7, v95
	v_mov_b32_e32 v6, v95
	v_mov_b32_e32 v5, v95
	v_mov_b32_e32 v4, v95
	v_mov_b32_e32 v3, v95
	v_mov_b32_e32 v2, v95
	v_mov_b32_e32 v1, v95
	v_mov_b32_e32 v0, v95
	s_cbranch_vccnz .LBB5_42
	v_mov_b32_e32 v0, 0
	v_lshl_add_u64 v[32:33], s[40:41], 0, v[112:113]
	v_lshl_add_u64 v[34:35], s[40:41], 0, v[114:115]
	v_lshl_add_u64 v[36:37], s[42:43], 0, v[116:117]
	v_lshl_add_u64 v[38:39], s[42:43], 0, v[118:119]
	v_lshl_add_u64 v[40:41], s[42:43], 0, v[120:121]
	v_lshl_add_u64 v[42:43], s[42:43], 0, v[122:123]
	s_mov_b32 s75, 0
	s_mov_b64 s[44:45], 0
	v_mov_b32_e32 v1, v0
	v_mov_b32_e32 v2, v0
	v_mov_b32_e32 v3, v0
	v_mov_b32_e32 v4, v0
	v_mov_b32_e32 v5, v0
	v_mov_b32_e32 v6, v0
	v_mov_b32_e32 v7, v0
	v_mov_b32_e32 v16, v0
	v_mov_b32_e32 v17, v0
	v_mov_b32_e32 v18, v0
	v_mov_b32_e32 v19, v0
	v_mov_b32_e32 v20, v0
	v_mov_b32_e32 v21, v0
	v_mov_b32_e32 v22, v0
	v_mov_b32_e32 v23, v0
	v_mov_b32_e32 v48, v0
	v_mov_b32_e32 v49, v0
	v_mov_b32_e32 v50, v0
	v_mov_b32_e32 v51, v0
	v_mov_b32_e32 v52, v0
	v_mov_b32_e32 v53, v0
	v_mov_b32_e32 v54, v0
	v_mov_b32_e32 v55, v0
	v_mov_b32_e32 v80, v0
	v_mov_b32_e32 v81, v0
	v_mov_b32_e32 v82, v0
	v_mov_b32_e32 v83, v0
	v_mov_b32_e32 v84, v0
	v_mov_b32_e32 v85, v0
	v_mov_b32_e32 v86, v0
	v_mov_b32_e32 v87, v0
	v_mov_b32_e32 v8, v0
	v_mov_b32_e32 v9, v0
	v_mov_b32_e32 v10, v0
	v_mov_b32_e32 v11, v0
	v_mov_b32_e32 v12, v0
	v_mov_b32_e32 v13, v0
	v_mov_b32_e32 v14, v0
	v_mov_b32_e32 v15, v0
	v_mov_b32_e32 v24, v0
	v_mov_b32_e32 v25, v0
	v_mov_b32_e32 v26, v0
	v_mov_b32_e32 v27, v0
	v_mov_b32_e32 v28, v0
	v_mov_b32_e32 v29, v0
	v_mov_b32_e32 v30, v0
	v_mov_b32_e32 v31, v0
	v_mov_b32_e32 v72, v0
	v_mov_b32_e32 v73, v0
	v_mov_b32_e32 v74, v0
	v_mov_b32_e32 v75, v0
	v_mov_b32_e32 v76, v0
	v_mov_b32_e32 v77, v0
	v_mov_b32_e32 v78, v0
	v_mov_b32_e32 v79, v0
	v_mov_b32_e32 v88, v0
	v_mov_b32_e32 v89, v0
	v_mov_b32_e32 v90, v0
	v_mov_b32_e32 v91, v0
	v_mov_b32_e32 v92, v0
	v_mov_b32_e32 v93, v0
	v_mov_b32_e32 v94, v0
	v_mov_b32_e32 v95, v0
	s_cmp_eq_u32 s78, 1
	s_cbranch_scc1 .Lg_loop

.Lg_loop:
	s_add_u32 s46, s40, s44
	s_addc_u32 s47, s41, s45
	s_add_u32 s46, s46, 0x180
	s_addc_u32 s47, s47, 0
	s_add_u32 s48, s42, s44
	s_addc_u32 s49, s43, s45
	s_add_u32 s76, s48, 0x180
	s_addc_u32 s77, s49, 0
	s_cmp_eq_u32 s67, s75
	s_cselect_b32 s49, s7, s47
	s_cselect_b32 s48, s6, s46
	s_cselect_b32 s47, s5, s77
	s_cselect_b32 s46, s4, s76
	s_add_i32 s76, s19, s54
	v_lshl_add_u64 v[126:127], v[32:33], 0, s[44:45]
	s_mov_b32 m0, s76
	ds_read_b128 v[44:47], v130 offset:16384
	ds_read_b128 v[56:59], v130 offset:17408
	ds_read_b128 v[60:63], v130 offset:18432
	ds_read_b128 v[64:67], v130 offset:19456
	ds_read_b128 v[68:71], v131
	ds_read_b128 v[96:99], v131 offset:1024
	ds_read_b128 v[136:139], v131 offset:2048
	ds_read_b128 v[140:143], v131 offset:3072
	ds_read_b128 v[144:147], v131 offset:4096
	ds_read_b128 v[148:151], v131 offset:5120
	ds_read_b128 v[152:155], v131 offset:6144
	ds_read_b128 v[156:159], v131 offset:7168
	global_load_lds_dwordx4 v[126:127], off
	v_lshl_add_u64 v[126:127], v[34:35], 0, s[44:45]
	s_add_i32 m0, s76, 0x2000
	s_add_i32 s76, s27, s54
	global_load_lds_dwordx4 v[126:127], off
	v_lshl_add_u64 v[126:127], v[36:37], 0, s[44:45]
	s_mov_b32 m0, s76
	s_nop 0
	global_load_lds_dwordx4 v[126:127], off
	v_lshl_add_u64 v[126:127], v[38:39], 0, s[44:45]
	s_add_i32 m0, s76, 0x2000
	s_nop 0
	global_load_lds_dwordx4 v[126:127], off
	s_barrier
	s_waitcnt lgkmcnt(0)
	s_setprio 1
	s_waitcnt lgkmcnt(0)
	v_mfma_f32_16x16x32_f16 v[92:95], v[44:47], v[68:71], v[92:95]
	v_and_b32_e32 v240, 0x7fffffff, v176
	v_and_b32_e32 v241, 0x7fffffff, v177
	v_mfma_f32_16x16x32_f16 v[88:91], v[60:63], v[68:71], v[88:91]
	v_pk_fma_f32 v[242:243], v[240:241], s[80:81], 1.0 op_sel_hi:[1,0,0]
	v_pk_mul_f32 v[246:247], v[176:177], v[176:177]
	v_mfma_f32_16x16x32_f16 v[76:79], v[44:47], v[136:139], v[76:79]
	v_rcp_f32_e32 v242, v242
	v_rcp_f32_e32 v243, v243
	v_mfma_f32_16x16x32_f16 v[72:75], v[60:63], v[136:139], v[72:75]
	v_pk_mul_f32 v[246:247], v[246:247], s[90:91] op_sel_hi:[1,0]
	v_pk_fma_f32 v[244:245], v[242:243], s[82:83], v[248:249] op_sel_hi:[1,0,1]
	v_mfma_f32_16x16x32_f16 v[28:31], v[44:47], v[144:147], v[28:31]
	v_exp_f32_e32 v246, v246
	v_exp_f32_e32 v247, v247
	v_mfma_f32_16x16x32_f16 v[24:27], v[60:63], v[144:147], v[24:27]
	v_pk_fma_f32 v[244:245], v[242:243], v[244:245], s[84:85] op_sel_hi:[1,1,0]
	v_pk_fma_f32 v[244:245], v[242:243], v[244:245], s[86:87] op_sel_hi:[1,1,0]
	v_mfma_f32_16x16x32_f16 v[12:15], v[44:47], v[152:155], v[12:15]
	v_pk_fma_f32 v[244:245], v[242:243], v[244:245], s[88:89] op_sel_hi:[1,1,0]
	v_pk_mul_f32 v[244:245], v[242:243], v[244:245]
	v_mfma_f32_16x16x32_f16 v[8:11], v[60:63], v[152:155], v[8:11]
	v_max_f32_e32 v242, 0, v176
	v_max_f32_e32 v243, 0, v177
	v_mfma_f32_16x16x32_f16 v[92:95], v[56:59], v[96:99], v[92:95]
	v_pk_mul_f32 v[244:245], v[244:245], v[246:247]
	v_pk_fma_f32 v[244:245], v[240:241], v[244:245], v[242:243] neg_lo:[1,0,0] neg_hi:[1,0,0]
	v_mfma_f32_16x16x32_f16 v[88:91], v[64:67], v[96:99], v[88:91]
	v_cvt_pk_f16_f32 v176, v244, v245
	v_and_b32_e32 v240, 0x7fffffff, v178
	v_mfma_f32_16x16x32_f16 v[76:79], v[56:59], v[140:143], v[76:79]
	v_and_b32_e32 v241, 0x7fffffff, v179
	v_pk_fma_f32 v[242:243], v[240:241], s[80:81], 1.0 op_sel_hi:[1,0,0]
	v_mfma_f32_16x16x32_f16 v[72:75], v[64:67], v[140:143], v[72:75]
	v_pk_mul_f32 v[246:247], v[178:179], v[178:179]
	v_rcp_f32_e32 v242, v242
	v_mfma_f32_16x16x32_f16 v[28:31], v[56:59], v[148:151], v[28:31]
	v_rcp_f32_e32 v243, v243
	v_pk_mul_f32 v[246:247], v[246:247], s[90:91] op_sel_hi:[1,0]
	v_mfma_f32_16x16x32_f16 v[24:27], v[64:67], v[148:151], v[24:27]
	v_pk_fma_f32 v[244:245], v[242:243], s[82:83], v[248:249] op_sel_hi:[1,0,1]
	v_exp_f32_e32 v246, v246
	v_mfma_f32_16x16x32_f16 v[12:15], v[56:59], v[156:159], v[12:15]
	v_exp_f32_e32 v247, v247
	v_pk_fma_f32 v[244:245], v[242:243], v[244:245], s[84:85] op_sel_hi:[1,1,0]
	v_mfma_f32_16x16x32_f16 v[8:11], v[64:67], v[156:159], v[8:11]
	v_pk_fma_f32 v[244:245], v[242:243], v[244:245], s[86:87] op_sel_hi:[1,1,0]
	v_pk_fma_f32 v[244:245], v[242:243], v[244:245], s[88:89] op_sel_hi:[1,1,0]
	s_setprio 0
	s_barrier
	s_add_i32 s76, s68, s54
	v_lshl_add_u64 v[126:127], v[40:41], 0, s[44:45]
	s_mov_b32 m0, s76
	ds_read_b128 v[44:47], v130 offset:32768
	ds_read_b128 v[56:59], v130 offset:33792
	ds_read_b128 v[60:63], v130 offset:34816
	ds_read_b128 v[64:67], v130 offset:35840
	global_load_lds_dwordx4 v[126:127], off
	v_lshl_add_u64 v[126:127], v[42:43], 0, s[44:45]
	s_add_i32 m0, s76, 0x2000
	s_nop 0
	global_load_lds_dwordx4 v[126:127], off
	s_waitcnt vmcnt(6)
	s_barrier
	s_waitcnt lgkmcnt(0)
	s_setprio 1
	s_waitcnt lgkmcnt(0)
	v_mfma_f32_16x16x32_f16 v[84:87], v[44:47], v[68:71], v[84:87]
	v_pk_mul_f32 v[244:245], v[242:243], v[244:245]
	v_max_f32_e32 v242, 0, v178
	v_mfma_f32_16x16x32_f16 v[52:55], v[44:47], v[136:139], v[52:55]
	v_max_f32_e32 v243, 0, v179
	v_pk_mul_f32 v[244:245], v[244:245], v[246:247]
	v_mfma_f32_16x16x32_f16 v[48:51], v[60:63], v[136:139], v[48:51]
	v_pk_fma_f32 v[244:245], v[240:241], v[244:245], v[242:243] neg_lo:[1,0,0] neg_hi:[1,0,0]
	v_cvt_pk_f16_f32 v177, v244, v245
	v_mfma_f32_16x16x32_f16 v[20:23], v[44:47], v[144:147], v[20:23]
	v_and_b32_e32 v240, 0x7fffffff, v180
	v_and_b32_e32 v241, 0x7fffffff, v181
	v_mfma_f32_16x16x32_f16 v[16:19], v[60:63], v[144:147], v[16:19]
	v_pk_fma_f32 v[242:243], v[240:241], s[80:81], 1.0 op_sel_hi:[1,0,0]
	v_pk_mul_f32 v[246:247], v[180:181], v[180:181]
	v_mfma_f32_16x16x32_f16 v[4:7], v[44:47], v[152:155], v[4:7]
	v_rcp_f32_e32 v242, v242
	v_rcp_f32_e32 v243, v243
	v_mfma_f32_16x16x32_f16 v[0:3], v[60:63], v[152:155], v[0:3]
	v_pk_mul_f32 v[246:247], v[246:247], s[90:91] op_sel_hi:[1,0]
	v_pk_fma_f32 v[244:245], v[242:243], s[82:83], v[248:249] op_sel_hi:[1,0,1]
	v_mfma_f32_16x16x32_f16 v[84:87], v[56:59], v[96:99], v[84:87]
	v_exp_f32_e32 v246, v246
	v_exp_f32_e32 v247, v247
	v_mfma_f32_16x16x32_f16 v[68:71], v[60:63], v[68:71], v[80:83]
	v_pk_fma_f32 v[244:245], v[242:243], v[244:245], s[84:85] op_sel_hi:[1,1,0]
	v_pk_fma_f32 v[244:245], v[242:243], v[244:245], s[86:87] op_sel_hi:[1,1,0]
	v_mfma_f32_16x16x32_f16 v[52:55], v[56:59], v[140:143], v[52:55]
	v_pk_fma_f32 v[244:245], v[242:243], v[244:245], s[88:89] op_sel_hi:[1,1,0]
	v_pk_mul_f32 v[244:245], v[242:243], v[244:245]
	v_mfma_f32_16x16x32_f16 v[48:51], v[64:67], v[140:143], v[48:51]
	v_max_f32_e32 v242, 0, v180
	v_max_f32_e32 v243, 0, v181
	v_mfma_f32_16x16x32_f16 v[20:23], v[56:59], v[148:151], v[20:23]
	v_pk_mul_f32 v[244:245], v[244:245], v[246:247]
	v_pk_fma_f32 v[244:245], v[240:241], v[244:245], v[242:243] neg_lo:[1,0,0] neg_hi:[1,0,0]
	v_mfma_f32_16x16x32_f16 v[16:19], v[64:67], v[148:151], v[16:19]
	v_cvt_pk_f16_f32 v178, v244, v245
	v_and_b32_e32 v240, 0x7fffffff, v182
	v_mfma_f32_16x16x32_f16 v[4:7], v[56:59], v[156:159], v[4:7]
	v_and_b32_e32 v241, 0x7fffffff, v183
	v_pk_fma_f32 v[242:243], v[240:241], s[80:81], 1.0 op_sel_hi:[1,0,0]
	v_mfma_f32_16x16x32_f16 v[0:3], v[64:67], v[156:159], v[0:3]
	v_pk_mul_f32 v[246:247], v[182:183], v[182:183]
	v_rcp_f32_e32 v242, v242
	v_mfma_f32_16x16x32_f16 v[68:71], v[64:67], v[96:99], v[68:71]
	v_rcp_f32_e32 v243, v243
	v_pk_mul_f32 v[246:247], v[246:247], s[90:91] op_sel_hi:[1,0]
	s_setprio 0
	s_barrier
	s_add_i32 s76, 0, 0x10000
	s_mov_b32 m0, s57
	v_add_u32_e32 v64, s76, v128
	v_lshl_add_u64 v[126:127], s[48:49], 0, v[100:101]
	ds_read_b128 v[44:47], v64
	ds_read_b128 v[56:59], v64 offset:1024
	ds_read_b128 v[60:63], v64 offset:2048
	ds_read_b128 v[64:67], v64 offset:3072
	ds_read_b128 v[80:83], v131 offset:49152
	ds_read_b128 v[96:99], v131 offset:50176
	ds_read_b128 v[136:139], v131 offset:51200
	ds_read_b128 v[140:143], v131 offset:52224
	ds_read_b128 v[144:147], v131 offset:53248
	ds_read_b128 v[148:151], v131 offset:54272
	ds_read_b128 v[152:155], v131 offset:55296
	ds_read_b128 v[156:159], v131 offset:56320
	global_load_lds_dwordx4 v[126:127], off
	v_lshl_add_u64 v[160:161], s[48:49], 0, v[104:105]
	s_mov_b32 m0, s58
	v_lshl_add_u64 v[162:163], s[46:47], 0, v[102:103]
	global_load_lds_dwordx4 v[160:161], off
	s_mov_b32 m0, s59
	v_lshl_add_u64 v[164:165], s[46:47], 0, v[106:107]
	global_load_lds_dwordx4 v[162:163], off
	s_mov_b32 m0, s60
	s_nop 0
	global_load_lds_dwordx4 v[164:165], off
	s_barrier
	s_waitcnt lgkmcnt(0)
	s_setprio 1
	s_waitcnt lgkmcnt(0)
	v_mfma_f32_16x16x32_f16 v[92:95], v[44:47], v[80:83], v[92:95]
	v_pk_fma_f32 v[244:245], v[242:243], s[82:83], v[248:249] op_sel_hi:[1,0,1]
	v_exp_f32_e32 v246, v246
	v_mfma_f32_16x16x32_f16 v[88:91], v[60:63], v[80:83], v[88:91]
	v_exp_f32_e32 v247, v247
	v_pk_fma_f32 v[244:245], v[242:243], v[244:245], s[84:85] op_sel_hi:[1,1,0]
	v_mfma_f32_16x16x32_f16 v[76:79], v[44:47], v[136:139], v[76:79]
	v_pk_fma_f32 v[244:245], v[242:243], v[244:245], s[86:87] op_sel_hi:[1,1,0]
	v_pk_fma_f32 v[244:245], v[242:243], v[244:245], s[88:89] op_sel_hi:[1,1,0]
	v_mfma_f32_16x16x32_f16 v[72:75], v[60:63], v[136:139], v[72:75]
	v_pk_mul_f32 v[244:245], v[242:243], v[244:245]
	v_max_f32_e32 v242, 0, v182
	v_mfma_f32_16x16x32_f16 v[28:31], v[44:47], v[144:147], v[28:31]
	v_max_f32_e32 v243, 0, v183
	v_pk_mul_f32 v[244:245], v[244:245], v[246:247]
	v_mfma_f32_16x16x32_f16 v[24:27], v[60:63], v[144:147], v[24:27]
	v_pk_fma_f32 v[244:245], v[240:241], v[244:245], v[242:243] neg_lo:[1,0,0] neg_hi:[1,0,0]
	v_cvt_pk_f16_f32 v179, v244, v245
	v_mfma_f32_16x16x32_f16 v[12:15], v[44:47], v[152:155], v[12:15]
	global_store_dwordx4 v[250:251], v[176:179], off sc1
	v_and_b32_e32 v240, 0x7fffffff, v184
	v_mfma_f32_16x16x32_f16 v[8:11], v[60:63], v[152:155], v[8:11]
	v_and_b32_e32 v241, 0x7fffffff, v185
	v_pk_fma_f32 v[242:243], v[240:241], s[80:81], 1.0 op_sel_hi:[1,0,0]
	v_mfma_f32_16x16x32_f16 v[92:95], v[56:59], v[96:99], v[92:95]
	v_pk_mul_f32 v[246:247], v[184:185], v[184:185]
	v_rcp_f32_e32 v242, v242
	v_mfma_f32_16x16x32_f16 v[88:91], v[64:67], v[96:99], v[88:91]
	v_rcp_f32_e32 v243, v243
	v_pk_mul_f32 v[246:247], v[246:247], s[90:91] op_sel_hi:[1,0]
	v_mfma_f32_16x16x32_f16 v[76:79], v[56:59], v[140:143], v[76:79]
	v_pk_fma_f32 v[244:245], v[242:243], s[82:83], v[248:249] op_sel_hi:[1,0,1]
	v_exp_f32_e32 v246, v246
	v_mfma_f32_16x16x32_f16 v[72:75], v[64:67], v[140:143], v[72:75]
	v_exp_f32_e32 v247, v247
	v_pk_fma_f32 v[244:245], v[242:243], v[244:245], s[84:85] op_sel_hi:[1,1,0]
	v_mfma_f32_16x16x32_f16 v[28:31], v[56:59], v[148:151], v[28:31]
	v_pk_fma_f32 v[244:245], v[242:243], v[244:245], s[86:87] op_sel_hi:[1,1,0]
	v_pk_fma_f32 v[244:245], v[242:243], v[244:245], s[88:89] op_sel_hi:[1,1,0]
	v_mfma_f32_16x16x32_f16 v[24:27], v[64:67], v[148:151], v[24:27]
	v_pk_mul_f32 v[244:245], v[242:243], v[244:245]
	v_max_f32_e32 v242, 0, v184
	v_mfma_f32_16x16x32_f16 v[12:15], v[56:59], v[156:159], v[12:15]
	v_max_f32_e32 v243, 0, v185
	v_pk_mul_f32 v[244:245], v[244:245], v[246:247]
	v_mfma_f32_16x16x32_f16 v[8:11], v[64:67], v[156:159], v[8:11]
	v_pk_fma_f32 v[244:245], v[240:241], v[244:245], v[242:243] neg_lo:[1,0,0] neg_hi:[1,0,0]
	v_cvt_pk_f16_f32 v184, v244, v245
	s_setprio 0
	s_barrier
	s_add_i32 s48, 0, 0x14000
	s_add_u32 s46, s46, s10
	s_addc_u32 s47, s47, s11
	s_mov_b32 m0, s61
	v_add_u32_e32 v64, s48, v128
	v_lshl_add_u64 v[166:167], s[46:47], 0, v[102:103]
	ds_read_b128 v[44:47], v64
	ds_read_b128 v[56:59], v64 offset:1024
	ds_read_b128 v[60:63], v64 offset:2048
	ds_read_b128 v[64:67], v64 offset:3072
	global_load_lds_dwordx4 v[166:167], off
	v_lshl_add_u64 v[168:169], s[46:47], 0, v[106:107]
	s_mov_b32 m0, s62
	s_nop 0
	global_load_lds_dwordx4 v[168:169], off
	s_waitcnt vmcnt(7)
	s_barrier
	s_waitcnt lgkmcnt(0)
	s_setprio 1
	s_waitcnt lgkmcnt(0)
	v_mfma_f32_16x16x32_f16 v[84:87], v[44:47], v[80:83], v[84:87]
	v_and_b32_e32 v240, 0x7fffffff, v186
	v_and_b32_e32 v241, 0x7fffffff, v187
	v_mfma_f32_16x16x32_f16 v[52:55], v[44:47], v[136:139], v[52:55]
	v_pk_fma_f32 v[242:243], v[240:241], s[80:81], 1.0 op_sel_hi:[1,0,0]
	v_pk_mul_f32 v[246:247], v[186:187], v[186:187]
	v_mfma_f32_16x16x32_f16 v[48:51], v[60:63], v[136:139], v[48:51]
	v_rcp_f32_e32 v242, v242
	v_rcp_f32_e32 v243, v243
	v_mfma_f32_16x16x32_f16 v[20:23], v[44:47], v[144:147], v[20:23]
	v_pk_mul_f32 v[246:247], v[246:247], s[90:91] op_sel_hi:[1,0]
	v_pk_fma_f32 v[244:245], v[242:243], s[82:83], v[248:249] op_sel_hi:[1,0,1]
	v_mfma_f32_16x16x32_f16 v[16:19], v[60:63], v[144:147], v[16:19]
	v_exp_f32_e32 v246, v246
	v_exp_f32_e32 v247, v247
	v_mfma_f32_16x16x32_f16 v[4:7], v[44:47], v[152:155], v[4:7]
	v_pk_fma_f32 v[244:245], v[242:243], v[244:245], s[84:85] op_sel_hi:[1,1,0]
	v_pk_fma_f32 v[244:245], v[242:243], v[244:245], s[86:87] op_sel_hi:[1,1,0]
	v_mfma_f32_16x16x32_f16 v[0:3], v[60:63], v[152:155], v[0:3]
	v_pk_fma_f32 v[244:245], v[242:243], v[244:245], s[88:89] op_sel_hi:[1,1,0]
	v_pk_mul_f32 v[244:245], v[242:243], v[244:245]
	v_mfma_f32_16x16x32_f16 v[84:87], v[56:59], v[96:99], v[84:87]
	v_max_f32_e32 v242, 0, v186
	v_max_f32_e32 v243, 0, v187
	v_mfma_f32_16x16x32_f16 v[68:71], v[60:63], v[80:83], v[68:71]
	v_pk_mul_f32 v[244:245], v[244:245], v[246:247]
	v_pk_fma_f32 v[244:245], v[240:241], v[244:245], v[242:243] neg_lo:[1,0,0] neg_hi:[1,0,0]
	v_mfma_f32_16x16x32_f16 v[52:55], v[56:59], v[140:143], v[52:55]
	v_cvt_pk_f16_f32 v185, v244, v245
	v_and_b32_e32 v240, 0x7fffffff, v188
	v_mfma_f32_16x16x32_f16 v[48:51], v[64:67], v[140:143], v[48:51]
	v_and_b32_e32 v241, 0x7fffffff, v189
	v_pk_fma_f32 v[242:243], v[240:241], s[80:81], 1.0 op_sel_hi:[1,0,0]
	v_mfma_f32_16x16x32_f16 v[20:23], v[56:59], v[148:151], v[20:23]
	v_pk_mul_f32 v[246:247], v[188:189], v[188:189]
	v_rcp_f32_e32 v242, v242
	v_mfma_f32_16x16x32_f16 v[16:19], v[64:67], v[148:151], v[16:19]
	v_rcp_f32_e32 v243, v243
	v_pk_mul_f32 v[246:247], v[246:247], s[90:91] op_sel_hi:[1,0]
	v_mfma_f32_16x16x32_f16 v[4:7], v[56:59], v[156:159], v[4:7]
	v_pk_fma_f32 v[244:245], v[242:243], s[82:83], v[248:249] op_sel_hi:[1,0,1]
	v_exp_f32_e32 v246, v246
	v_mfma_f32_16x16x32_f16 v[0:3], v[64:67], v[156:159], v[0:3]
	v_exp_f32_e32 v247, v247
	v_pk_fma_f32 v[244:245], v[242:243], v[244:245], s[84:85] op_sel_hi:[1,1,0]
	v_mfma_f32_16x16x32_f16 v[68:71], v[64:67], v[96:99], v[68:71]
	v_pk_fma_f32 v[244:245], v[242:243], v[244:245], s[86:87] op_sel_hi:[1,1,0]
	v_pk_fma_f32 v[244:245], v[242:243], v[244:245], s[88:89] op_sel_hi:[1,1,0]
	s_setprio 0
	s_barrier
	s_mov_b32 m0, s64
	v_lshl_add_u64 v[126:127], v[126:127], 0, s[22:23]
	ds_read_b128 v[44:47], v132
	ds_read_b128 v[56:59], v132 offset:1024
	ds_read_b128 v[60:63], v132 offset:2048
	ds_read_b128 v[64:67], v132 offset:3072
	ds_read_b128 v[80:83], v133
	ds_read_b128 v[96:99], v133 offset:1024
	ds_read_b128 v[136:139], v133 offset:2048
	ds_read_b128 v[140:143], v133 offset:3072
	ds_read_b128 v[144:147], v133 offset:4096
	ds_read_b128 v[148:151], v133 offset:5120
	ds_read_b128 v[152:155], v133 offset:6144
	ds_read_b128 v[156:159], v133 offset:7168
	global_load_lds_dwordx4 v[126:127], off
	v_lshl_add_u64 v[126:127], v[160:161], 0, s[22:23]
	s_mov_b32 m0, s65
	s_add_i32 s46, s76, s54
	global_load_lds_dwordx4 v[126:127], off
	v_lshl_add_u64 v[126:127], v[162:163], 0, s[22:23]
	s_mov_b32 m0, s46
	s_nop 0
	global_load_lds_dwordx4 v[126:127], off
	v_lshl_add_u64 v[126:127], v[164:165], 0, s[22:23]
	s_add_i32 m0, s46, 0x2000
	s_nop 0
	global_load_lds_dwordx4 v[126:127], off
	s_barrier
	s_waitcnt lgkmcnt(0)
	s_setprio 1
	s_waitcnt lgkmcnt(0)
	v_mfma_f32_16x16x32_f16 v[92:95], v[44:47], v[80:83], v[92:95]
	v_pk_mul_f32 v[244:245], v[242:243], v[244:245]
	v_max_f32_e32 v242, 0, v188
	v_mfma_f32_16x16x32_f16 v[88:91], v[60:63], v[80:83], v[88:91]
	v_max_f32_e32 v243, 0, v189
	v_pk_mul_f32 v[244:245], v[244:245], v[246:247]
	v_mfma_f32_16x16x32_f16 v[76:79], v[44:47], v[136:139], v[76:79]
	v_pk_fma_f32 v[244:245], v[240:241], v[244:245], v[242:243] neg_lo:[1,0,0] neg_hi:[1,0,0]
	v_cvt_pk_f16_f32 v186, v244, v245
	v_mfma_f32_16x16x32_f16 v[72:75], v[60:63], v[136:139], v[72:75]
	v_and_b32_e32 v240, 0x7fffffff, v190
	v_and_b32_e32 v241, 0x7fffffff, v191
	v_mfma_f32_16x16x32_f16 v[28:31], v[44:47], v[144:147], v[28:31]
	v_pk_fma_f32 v[242:243], v[240:241], s[80:81], 1.0 op_sel_hi:[1,0,0]
	v_pk_mul_f32 v[246:247], v[190:191], v[190:191]
	v_mfma_f32_16x16x32_f16 v[24:27], v[60:63], v[144:147], v[24:27]
	v_rcp_f32_e32 v242, v242
	v_rcp_f32_e32 v243, v243
	v_mfma_f32_16x16x32_f16 v[12:15], v[44:47], v[152:155], v[12:15]
	v_pk_mul_f32 v[246:247], v[246:247], s[90:91] op_sel_hi:[1,0]
	v_pk_fma_f32 v[244:245], v[242:243], s[82:83], v[248:249] op_sel_hi:[1,0,1]
	v_mfma_f32_16x16x32_f16 v[8:11], v[60:63], v[152:155], v[8:11]
	v_exp_f32_e32 v246, v246
	v_exp_f32_e32 v247, v247
	v_mfma_f32_16x16x32_f16 v[92:95], v[56:59], v[96:99], v[92:95]
	v_pk_fma_f32 v[244:245], v[242:243], v[244:245], s[84:85] op_sel_hi:[1,1,0]
	v_pk_fma_f32 v[244:245], v[242:243], v[244:245], s[86:87] op_sel_hi:[1,1,0]
	v_mfma_f32_16x16x32_f16 v[88:91], v[64:67], v[96:99], v[88:91]
	v_pk_fma_f32 v[244:245], v[242:243], v[244:245], s[88:89] op_sel_hi:[1,1,0]
	v_pk_mul_f32 v[244:245], v[242:243], v[244:245]
	v_mfma_f32_16x16x32_f16 v[76:79], v[56:59], v[140:143], v[76:79]
	v_max_f32_e32 v242, 0, v190
	v_max_f32_e32 v243, 0, v191
	v_mfma_f32_16x16x32_f16 v[72:75], v[64:67], v[140:143], v[72:75]
	v_pk_mul_f32 v[244:245], v[244:245], v[246:247]
	v_pk_fma_f32 v[244:245], v[240:241], v[244:245], v[242:243] neg_lo:[1,0,0] neg_hi:[1,0,0]
	v_mfma_f32_16x16x32_f16 v[28:31], v[56:59], v[148:151], v[28:31]
	v_cvt_pk_f16_f32 v187, v244, v245
	global_store_dwordx4 v[250:251], v[184:187], off offset:256 sc1
	v_mfma_f32_16x16x32_f16 v[24:27], v[64:67], v[148:151], v[24:27]
	v_and_b32_e32 v240, 0x7fffffff, v192
	v_and_b32_e32 v241, 0x7fffffff, v193
	v_mfma_f32_16x16x32_f16 v[12:15], v[56:59], v[156:159], v[12:15]
	v_pk_fma_f32 v[242:243], v[240:241], s[80:81], 1.0 op_sel_hi:[1,0,0]
	v_pk_mul_f32 v[246:247], v[192:193], v[192:193]
	v_mfma_f32_16x16x32_f16 v[8:11], v[64:67], v[156:159], v[8:11]
	v_rcp_f32_e32 v242, v242
	v_rcp_f32_e32 v243, v243
	s_setprio 0
	s_barrier
	s_add_i32 s46, s48, s54
	v_lshl_add_u64 v[126:127], v[166:167], 0, s[22:23]
	s_mov_b32 m0, s46
	ds_read_b128 v[44:47], v134
	ds_read_b128 v[56:59], v134 offset:1024
	ds_read_b128 v[60:63], v134 offset:2048
	ds_read_b128 v[64:67], v134 offset:3072
	global_load_lds_dwordx4 v[126:127], off
	v_lshl_add_u64 v[126:127], v[168:169], 0, s[22:23]
	s_add_i32 m0, s46, 0x2000
	s_nop 0
	global_load_lds_dwordx4 v[126:127], off
	s_waitcnt vmcnt(7)
	s_barrier
	s_waitcnt lgkmcnt(0)
	s_setprio 1
	s_waitcnt lgkmcnt(0)
	v_mfma_f32_16x16x32_f16 v[84:87], v[44:47], v[80:83], v[84:87]
	v_pk_mul_f32 v[246:247], v[246:247], s[90:91] op_sel_hi:[1,0]
	v_pk_fma_f32 v[244:245], v[242:243], s[82:83], v[248:249] op_sel_hi:[1,0,1]
	v_mfma_f32_16x16x32_f16 v[68:71], v[60:63], v[80:83], v[68:71]
	v_exp_f32_e32 v246, v246
	v_exp_f32_e32 v247, v247
	v_mfma_f32_16x16x32_f16 v[52:55], v[44:47], v[136:139], v[52:55]
	v_pk_fma_f32 v[244:245], v[242:243], v[244:245], s[84:85] op_sel_hi:[1,1,0]
	v_pk_fma_f32 v[244:245], v[242:243], v[244:245], s[86:87] op_sel_hi:[1,1,0]
	v_mfma_f32_16x16x32_f16 v[48:51], v[60:63], v[136:139], v[48:51]
	v_pk_fma_f32 v[244:245], v[242:243], v[244:245], s[88:89] op_sel_hi:[1,1,0]
	v_pk_mul_f32 v[244:245], v[242:243], v[244:245]
	v_mfma_f32_16x16x32_f16 v[20:23], v[44:47], v[144:147], v[20:23]
	v_max_f32_e32 v242, 0, v192
	v_max_f32_e32 v243, 0, v193
	v_mfma_f32_16x16x32_f16 v[16:19], v[60:63], v[144:147], v[16:19]
	v_pk_mul_f32 v[244:245], v[244:245], v[246:247]
	v_pk_fma_f32 v[244:245], v[240:241], v[244:245], v[242:243] neg_lo:[1,0,0] neg_hi:[1,0,0]
	v_mfma_f32_16x16x32_f16 v[4:7], v[44:47], v[152:155], v[4:7]
	v_cvt_pk_f16_f32 v192, v244, v245
	v_and_b32_e32 v240, 0x7fffffff, v194
	v_mfma_f32_16x16x32_f16 v[0:3], v[60:63], v[152:155], v[0:3]
	v_and_b32_e32 v241, 0x7fffffff, v195
	v_pk_fma_f32 v[242:243], v[240:241], s[80:81], 1.0 op_sel_hi:[1,0,0]
	v_mfma_f32_16x16x32_f16 v[84:87], v[56:59], v[96:99], v[84:87]
	v_pk_mul_f32 v[246:247], v[194:195], v[194:195]
	v_rcp_f32_e32 v242, v242
	v_mfma_f32_16x16x32_f16 v[80:83], v[64:67], v[96:99], v[68:71]
	v_rcp_f32_e32 v243, v243
	v_pk_mul_f32 v[246:247], v[246:247], s[90:91] op_sel_hi:[1,0]
	v_mfma_f32_16x16x32_f16 v[52:55], v[56:59], v[140:143], v[52:55]
	v_pk_fma_f32 v[244:245], v[242:243], s[82:83], v[248:249] op_sel_hi:[1,0,1]
	v_exp_f32_e32 v246, v246
	v_mfma_f32_16x16x32_f16 v[48:51], v[64:67], v[140:143], v[48:51]
	v_exp_f32_e32 v247, v247
	v_pk_fma_f32 v[244:245], v[242:243], v[244:245], s[84:85] op_sel_hi:[1,1,0]
	v_mfma_f32_16x16x32_f16 v[20:23], v[56:59], v[148:151], v[20:23]
	v_pk_fma_f32 v[244:245], v[242:243], v[244:245], s[86:87] op_sel_hi:[1,1,0]
	v_pk_fma_f32 v[244:245], v[242:243], v[244:245], s[88:89] op_sel_hi:[1,1,0]
	v_mfma_f32_16x16x32_f16 v[16:19], v[64:67], v[148:151], v[16:19]
	v_pk_mul_f32 v[244:245], v[242:243], v[244:245]
	v_max_f32_e32 v242, 0, v194
	v_mfma_f32_16x16x32_f16 v[4:7], v[56:59], v[156:159], v[4:7]
	v_max_f32_e32 v243, 0, v195
	v_pk_mul_f32 v[244:245], v[244:245], v[246:247]
	v_mfma_f32_16x16x32_f16 v[0:3], v[64:67], v[156:159], v[0:3]
	v_pk_fma_f32 v[244:245], v[240:241], v[244:245], v[242:243] neg_lo:[1,0,0] neg_hi:[1,0,0]
	v_cvt_pk_f16_f32 v193, v244, v245
	s_setprio 0
	s_barrier
	s_add_i32 s75, s75, 3
	s_add_u32 s44, s44, 0x180
	s_addc_u32 s45, s45, 0
	s_add_u32 s46, s40, s44
	s_addc_u32 s47, s41, s45
	s_add_u32 s46, s46, 0x180
	s_addc_u32 s47, s47, 0
	s_add_u32 s48, s42, s44
	s_addc_u32 s49, s43, s45
	s_add_u32 s76, s48, 0x180
	s_addc_u32 s77, s49, 0
	s_cmp_eq_u32 s67, s75
	s_cselect_b32 s49, s7, s47
	s_cselect_b32 s48, s6, s46
	s_cselect_b32 s47, s5, s77
	s_cselect_b32 s46, s4, s76
	s_add_i32 s76, s19, s54
	v_lshl_add_u64 v[126:127], v[32:33], 0, s[44:45]
	s_mov_b32 m0, s76
	ds_read_b128 v[44:47], v130 offset:16384
	ds_read_b128 v[56:59], v130 offset:17408
	ds_read_b128 v[60:63], v130 offset:18432
	ds_read_b128 v[64:67], v130 offset:19456
	ds_read_b128 v[68:71], v131
	ds_read_b128 v[96:99], v131 offset:1024
	ds_read_b128 v[136:139], v131 offset:2048
	ds_read_b128 v[140:143], v131 offset:3072
	ds_read_b128 v[144:147], v131 offset:4096
	ds_read_b128 v[148:151], v131 offset:5120
	ds_read_b128 v[152:155], v131 offset:6144
	ds_read_b128 v[156:159], v131 offset:7168
	global_load_lds_dwordx4 v[126:127], off
	v_lshl_add_u64 v[126:127], v[34:35], 0, s[44:45]
	s_add_i32 m0, s76, 0x2000
	s_add_i32 s76, s27, s54
	global_load_lds_dwordx4 v[126:127], off
	v_lshl_add_u64 v[126:127], v[36:37], 0, s[44:45]
	s_mov_b32 m0, s76
	s_nop 0
	global_load_lds_dwordx4 v[126:127], off
	v_lshl_add_u64 v[126:127], v[38:39], 0, s[44:45]
	s_add_i32 m0, s76, 0x2000
	s_nop 0
	global_load_lds_dwordx4 v[126:127], off
	s_barrier
	s_waitcnt lgkmcnt(0)
	s_setprio 1
	s_waitcnt lgkmcnt(0)
	v_mfma_f32_16x16x32_f16 v[92:95], v[44:47], v[68:71], v[92:95]
	v_and_b32_e32 v240, 0x7fffffff, v196
	v_and_b32_e32 v241, 0x7fffffff, v197
	v_mfma_f32_16x16x32_f16 v[88:91], v[60:63], v[68:71], v[88:91]
	v_pk_fma_f32 v[242:243], v[240:241], s[80:81], 1.0 op_sel_hi:[1,0,0]
	v_pk_mul_f32 v[246:247], v[196:197], v[196:197]
	v_mfma_f32_16x16x32_f16 v[76:79], v[44:47], v[136:139], v[76:79]
	v_rcp_f32_e32 v242, v242
	v_rcp_f32_e32 v243, v243
	v_mfma_f32_16x16x32_f16 v[72:75], v[60:63], v[136:139], v[72:75]
	v_pk_mul_f32 v[246:247], v[246:247], s[90:91] op_sel_hi:[1,0]
	v_pk_fma_f32 v[244:245], v[242:243], s[82:83], v[248:249] op_sel_hi:[1,0,1]
	v_mfma_f32_16x16x32_f16 v[28:31], v[44:47], v[144:147], v[28:31]
	v_exp_f32_e32 v246, v246
	v_exp_f32_e32 v247, v247
	v_mfma_f32_16x16x32_f16 v[24:27], v[60:63], v[144:147], v[24:27]
	v_pk_fma_f32 v[244:245], v[242:243], v[244:245], s[84:85] op_sel_hi:[1,1,0]
	v_pk_fma_f32 v[244:245], v[242:243], v[244:245], s[86:87] op_sel_hi:[1,1,0]
	v_mfma_f32_16x16x32_f16 v[12:15], v[44:47], v[152:155], v[12:15]
	v_pk_fma_f32 v[244:245], v[242:243], v[244:245], s[88:89] op_sel_hi:[1,1,0]
	v_pk_mul_f32 v[244:245], v[242:243], v[244:245]
	v_mfma_f32_16x16x32_f16 v[8:11], v[60:63], v[152:155], v[8:11]
	v_max_f32_e32 v242, 0, v196
	v_max_f32_e32 v243, 0, v197
	v_mfma_f32_16x16x32_f16 v[92:95], v[56:59], v[96:99], v[92:95]
	v_pk_mul_f32 v[244:245], v[244:245], v[246:247]
	v_pk_fma_f32 v[244:245], v[240:241], v[244:245], v[242:243] neg_lo:[1,0,0] neg_hi:[1,0,0]
	v_mfma_f32_16x16x32_f16 v[88:91], v[64:67], v[96:99], v[88:91]
	v_cvt_pk_f16_f32 v194, v244, v245
	v_and_b32_e32 v240, 0x7fffffff, v198
	v_mfma_f32_16x16x32_f16 v[76:79], v[56:59], v[140:143], v[76:79]
	v_and_b32_e32 v241, 0x7fffffff, v199
	v_pk_fma_f32 v[242:243], v[240:241], s[80:81], 1.0 op_sel_hi:[1,0,0]
	v_mfma_f32_16x16x32_f16 v[72:75], v[64:67], v[140:143], v[72:75]
	v_pk_mul_f32 v[246:247], v[198:199], v[198:199]
	v_rcp_f32_e32 v242, v242
	v_mfma_f32_16x16x32_f16 v[28:31], v[56:59], v[148:151], v[28:31]
	v_rcp_f32_e32 v243, v243
	v_pk_mul_f32 v[246:247], v[246:247], s[90:91] op_sel_hi:[1,0]
	v_mfma_f32_16x16x32_f16 v[24:27], v[64:67], v[148:151], v[24:27]
	v_pk_fma_f32 v[244:245], v[242:243], s[82:83], v[248:249] op_sel_hi:[1,0,1]
	v_exp_f32_e32 v246, v246
	v_mfma_f32_16x16x32_f16 v[12:15], v[56:59], v[156:159], v[12:15]
	v_exp_f32_e32 v247, v247
	v_pk_fma_f32 v[244:245], v[242:243], v[244:245], s[84:85] op_sel_hi:[1,1,0]
	v_mfma_f32_16x16x32_f16 v[8:11], v[64:67], v[156:159], v[8:11]
	v_pk_fma_f32 v[244:245], v[242:243], v[244:245], s[86:87] op_sel_hi:[1,1,0]
	v_pk_fma_f32 v[244:245], v[242:243], v[244:245], s[88:89] op_sel_hi:[1,1,0]
	s_setprio 0
	s_barrier
	s_add_i32 s76, s68, s54
	v_lshl_add_u64 v[126:127], v[40:41], 0, s[44:45]
	s_mov_b32 m0, s76
	ds_read_b128 v[44:47], v130 offset:32768
	ds_read_b128 v[56:59], v130 offset:33792
	ds_read_b128 v[60:63], v130 offset:34816
	ds_read_b128 v[64:67], v130 offset:35840
	global_load_lds_dwordx4 v[126:127], off
	v_lshl_add_u64 v[126:127], v[42:43], 0, s[44:45]
	s_add_i32 m0, s76, 0x2000
	s_nop 0
	global_load_lds_dwordx4 v[126:127], off
	s_waitcnt vmcnt(6)
	s_barrier
	s_waitcnt lgkmcnt(0)
	s_setprio 1
	s_waitcnt lgkmcnt(0)
	v_mfma_f32_16x16x32_f16 v[84:87], v[44:47], v[68:71], v[84:87]
	v_pk_mul_f32 v[244:245], v[242:243], v[244:245]
	v_max_f32_e32 v242, 0, v198
	v_mfma_f32_16x16x32_f16 v[52:55], v[44:47], v[136:139], v[52:55]
	v_max_f32_e32 v243, 0, v199
	v_pk_mul_f32 v[244:245], v[244:245], v[246:247]
	v_mfma_f32_16x16x32_f16 v[48:51], v[60:63], v[136:139], v[48:51]
	v_pk_fma_f32 v[244:245], v[240:241], v[244:245], v[242:243] neg_lo:[1,0,0] neg_hi:[1,0,0]
	v_cvt_pk_f16_f32 v195, v244, v245
	v_mfma_f32_16x16x32_f16 v[20:23], v[44:47], v[144:147], v[20:23]
	v_lshl_add_u64 v[252:253], v[250:251], 0, s[92:93]
	global_store_dwordx4 v[252:253], v[192:195], off sc1
	v_mfma_f32_16x16x32_f16 v[16:19], v[60:63], v[144:147], v[16:19]
	v_and_b32_e32 v240, 0x7fffffff, v200
	v_and_b32_e32 v241, 0x7fffffff, v201
	v_mfma_f32_16x16x32_f16 v[4:7], v[44:47], v[152:155], v[4:7]
	v_pk_fma_f32 v[242:243], v[240:241], s[80:81], 1.0 op_sel_hi:[1,0,0]
	v_pk_mul_f32 v[246:247], v[200:201], v[200:201]
	v_mfma_f32_16x16x32_f16 v[0:3], v[60:63], v[152:155], v[0:3]
	v_rcp_f32_e32 v242, v242
	v_rcp_f32_e32 v243, v243
	v_mfma_f32_16x16x32_f16 v[84:87], v[56:59], v[96:99], v[84:87]
	v_pk_mul_f32 v[246:247], v[246:247], s[90:91] op_sel_hi:[1,0]
	v_pk_fma_f32 v[244:245], v[242:243], s[82:83], v[248:249] op_sel_hi:[1,0,1]
	v_mfma_f32_16x16x32_f16 v[68:71], v[60:63], v[68:71], v[80:83]
	v_exp_f32_e32 v246, v246
	v_exp_f32_e32 v247, v247
	v_mfma_f32_16x16x32_f16 v[52:55], v[56:59], v[140:143], v[52:55]
	v_pk_fma_f32 v[244:245], v[242:243], v[244:245], s[84:85] op_sel_hi:[1,1,0]
	v_pk_fma_f32 v[244:245], v[242:243], v[244:245], s[86:87] op_sel_hi:[1,1,0]
	v_mfma_f32_16x16x32_f16 v[48:51], v[64:67], v[140:143], v[48:51]
	v_pk_fma_f32 v[244:245], v[242:243], v[244:245], s[88:89] op_sel_hi:[1,1,0]
	v_pk_mul_f32 v[244:245], v[242:243], v[244:245]
	v_mfma_f32_16x16x32_f16 v[20:23], v[56:59], v[148:151], v[20:23]
	v_max_f32_e32 v242, 0, v200
	v_max_f32_e32 v243, 0, v201
	v_mfma_f32_16x16x32_f16 v[16:19], v[64:67], v[148:151], v[16:19]
	v_pk_mul_f32 v[244:245], v[244:245], v[246:247]
	v_pk_fma_f32 v[244:245], v[240:241], v[244:245], v[242:243] neg_lo:[1,0,0] neg_hi:[1,0,0]
	v_mfma_f32_16x16x32_f16 v[4:7], v[56:59], v[156:159], v[4:7]
	v_cvt_pk_f16_f32 v200, v244, v245
	v_and_b32_e32 v240, 0x7fffffff, v202
	v_mfma_f32_16x16x32_f16 v[0:3], v[64:67], v[156:159], v[0:3]
	v_and_b32_e32 v241, 0x7fffffff, v203
	v_pk_fma_f32 v[242:243], v[240:241], s[80:81], 1.0 op_sel_hi:[1,0,0]
	v_mfma_f32_16x16x32_f16 v[68:71], v[64:67], v[96:99], v[68:71]
	v_pk_mul_f32 v[246:247], v[202:203], v[202:203]
	v_rcp_f32_e32 v242, v242
	s_setprio 0
	s_barrier
	s_add_i32 s76, 0, 0x10000
	s_mov_b32 m0, s57
	v_add_u32_e32 v64, s76, v128
	v_lshl_add_u64 v[126:127], s[48:49], 0, v[100:101]
	ds_read_b128 v[44:47], v64
	ds_read_b128 v[56:59], v64 offset:1024
	ds_read_b128 v[60:63], v64 offset:2048
	ds_read_b128 v[64:67], v64 offset:3072
	ds_read_b128 v[80:83], v131 offset:49152
	ds_read_b128 v[96:99], v131 offset:50176
	ds_read_b128 v[136:139], v131 offset:51200
	ds_read_b128 v[140:143], v131 offset:52224
	ds_read_b128 v[144:147], v131 offset:53248
	ds_read_b128 v[148:151], v131 offset:54272
	ds_read_b128 v[152:155], v131 offset:55296
	ds_read_b128 v[156:159], v131 offset:56320
	global_load_lds_dwordx4 v[126:127], off
	v_lshl_add_u64 v[160:161], s[48:49], 0, v[104:105]
	s_mov_b32 m0, s58
	v_lshl_add_u64 v[162:163], s[46:47], 0, v[102:103]
	global_load_lds_dwordx4 v[160:161], off
	s_mov_b32 m0, s59
	v_lshl_add_u64 v[164:165], s[46:47], 0, v[106:107]
	global_load_lds_dwordx4 v[162:163], off
	s_mov_b32 m0, s60
	s_nop 0
	global_load_lds_dwordx4 v[164:165], off
	s_barrier
	s_waitcnt lgkmcnt(0)
	s_setprio 1
	s_waitcnt lgkmcnt(0)
	v_mfma_f32_16x16x32_f16 v[92:95], v[44:47], v[80:83], v[92:95]
	v_rcp_f32_e32 v243, v243
	v_pk_mul_f32 v[246:247], v[246:247], s[90:91] op_sel_hi:[1,0]
	v_mfma_f32_16x16x32_f16 v[88:91], v[60:63], v[80:83], v[88:91]
	v_pk_fma_f32 v[244:245], v[242:243], s[82:83], v[248:249] op_sel_hi:[1,0,1]
	v_exp_f32_e32 v246, v246
	v_mfma_f32_16x16x32_f16 v[76:79], v[44:47], v[136:139], v[76:79]
	v_exp_f32_e32 v247, v247
	v_pk_fma_f32 v[244:245], v[242:243], v[244:245], s[84:85] op_sel_hi:[1,1,0]
	v_mfma_f32_16x16x32_f16 v[72:75], v[60:63], v[136:139], v[72:75]
	v_pk_fma_f32 v[244:245], v[242:243], v[244:245], s[86:87] op_sel_hi:[1,1,0]
	v_pk_fma_f32 v[244:245], v[242:243], v[244:245], s[88:89] op_sel_hi:[1,1,0]
	v_mfma_f32_16x16x32_f16 v[28:31], v[44:47], v[144:147], v[28:31]
	v_pk_mul_f32 v[244:245], v[242:243], v[244:245]
	v_max_f32_e32 v242, 0, v202
	v_mfma_f32_16x16x32_f16 v[24:27], v[60:63], v[144:147], v[24:27]
	v_max_f32_e32 v243, 0, v203
	v_pk_mul_f32 v[244:245], v[244:245], v[246:247]
	v_mfma_f32_16x16x32_f16 v[12:15], v[44:47], v[152:155], v[12:15]
	v_pk_fma_f32 v[244:245], v[240:241], v[244:245], v[242:243] neg_lo:[1,0,0] neg_hi:[1,0,0]
	v_cvt_pk_f16_f32 v201, v244, v245
	v_mfma_f32_16x16x32_f16 v[8:11], v[60:63], v[152:155], v[8:11]
	v_and_b32_e32 v240, 0x7fffffff, v204
	v_and_b32_e32 v241, 0x7fffffff, v205
	v_mfma_f32_16x16x32_f16 v[92:95], v[56:59], v[96:99], v[92:95]
	v_pk_fma_f32 v[242:243], v[240:241], s[80:81], 1.0 op_sel_hi:[1,0,0]
	v_pk_mul_f32 v[246:247], v[204:205], v[204:205]
	v_mfma_f32_16x16x32_f16 v[88:91], v[64:67], v[96:99], v[88:91]
	v_rcp_f32_e32 v242, v242
	v_rcp_f32_e32 v243, v243
	v_mfma_f32_16x16x32_f16 v[76:79], v[56:59], v[140:143], v[76:79]
	v_pk_mul_f32 v[246:247], v[246:247], s[90:91] op_sel_hi:[1,0]
	v_pk_fma_f32 v[244:245], v[242:243], s[82:83], v[248:249] op_sel_hi:[1,0,1]
	v_mfma_f32_16x16x32_f16 v[72:75], v[64:67], v[140:143], v[72:75]
	v_exp_f32_e32 v246, v246
	v_exp_f32_e32 v247, v247
	v_mfma_f32_16x16x32_f16 v[28:31], v[56:59], v[148:151], v[28:31]
	v_pk_fma_f32 v[244:245], v[242:243], v[244:245], s[84:85] op_sel_hi:[1,1,0]
	v_pk_fma_f32 v[244:245], v[242:243], v[244:245], s[86:87] op_sel_hi:[1,1,0]
	v_mfma_f32_16x16x32_f16 v[24:27], v[64:67], v[148:151], v[24:27]
	v_pk_fma_f32 v[244:245], v[242:243], v[244:245], s[88:89] op_sel_hi:[1,1,0]
	v_pk_mul_f32 v[244:245], v[242:243], v[244:245]
	v_mfma_f32_16x16x32_f16 v[12:15], v[56:59], v[156:159], v[12:15]
	v_max_f32_e32 v242, 0, v204
	v_max_f32_e32 v243, 0, v205
	v_mfma_f32_16x16x32_f16 v[8:11], v[64:67], v[156:159], v[8:11]
	v_pk_mul_f32 v[244:245], v[244:245], v[246:247]
	v_pk_fma_f32 v[244:245], v[240:241], v[244:245], v[242:243] neg_lo:[1,0,0] neg_hi:[1,0,0]
	s_setprio 0
	s_barrier
	s_add_i32 s48, 0, 0x14000
	s_add_u32 s46, s46, s10
	s_addc_u32 s47, s47, s11
	s_mov_b32 m0, s61
	v_add_u32_e32 v64, s48, v128
	v_lshl_add_u64 v[166:167], s[46:47], 0, v[102:103]
	ds_read_b128 v[44:47], v64
	ds_read_b128 v[56:59], v64 offset:1024
	ds_read_b128 v[60:63], v64 offset:2048
	ds_read_b128 v[64:67], v64 offset:3072
	global_load_lds_dwordx4 v[166:167], off
	v_lshl_add_u64 v[168:169], s[46:47], 0, v[106:107]
	s_mov_b32 m0, s62
	s_nop 0
	global_load_lds_dwordx4 v[168:169], off
	s_waitcnt vmcnt(7)
	s_barrier
	s_waitcnt lgkmcnt(0)
	s_setprio 1
	s_waitcnt lgkmcnt(0)
	v_mfma_f32_16x16x32_f16 v[84:87], v[44:47], v[80:83], v[84:87]
	v_cvt_pk_f16_f32 v202, v244, v245
	v_and_b32_e32 v240, 0x7fffffff, v206
	v_mfma_f32_16x16x32_f16 v[52:55], v[44:47], v[136:139], v[52:55]
	v_and_b32_e32 v241, 0x7fffffff, v207
	v_pk_fma_f32 v[242:243], v[240:241], s[80:81], 1.0 op_sel_hi:[1,0,0]
	v_mfma_f32_16x16x32_f16 v[48:51], v[60:63], v[136:139], v[48:51]
	v_pk_mul_f32 v[246:247], v[206:207], v[206:207]
	v_rcp_f32_e32 v242, v242
	v_mfma_f32_16x16x32_f16 v[20:23], v[44:47], v[144:147], v[20:23]
	v_rcp_f32_e32 v243, v243
	v_pk_mul_f32 v[246:247], v[246:247], s[90:91] op_sel_hi:[1,0]
	v_mfma_f32_16x16x32_f16 v[16:19], v[60:63], v[144:147], v[16:19]
	v_pk_fma_f32 v[244:245], v[242:243], s[82:83], v[248:249] op_sel_hi:[1,0,1]
	v_exp_f32_e32 v246, v246
	v_mfma_f32_16x16x32_f16 v[4:7], v[44:47], v[152:155], v[4:7]
	v_exp_f32_e32 v247, v247
	v_pk_fma_f32 v[244:245], v[242:243], v[244:245], s[84:85] op_sel_hi:[1,1,0]
	v_mfma_f32_16x16x32_f16 v[0:3], v[60:63], v[152:155], v[0:3]
	v_pk_fma_f32 v[244:245], v[242:243], v[244:245], s[86:87] op_sel_hi:[1,1,0]
	v_pk_fma_f32 v[244:245], v[242:243], v[244:245], s[88:89] op_sel_hi:[1,1,0]
	v_mfma_f32_16x16x32_f16 v[84:87], v[56:59], v[96:99], v[84:87]
	v_pk_mul_f32 v[244:245], v[242:243], v[244:245]
	v_max_f32_e32 v242, 0, v206
	v_mfma_f32_16x16x32_f16 v[68:71], v[60:63], v[80:83], v[68:71]
	v_max_f32_e32 v243, 0, v207
	v_pk_mul_f32 v[244:245], v[244:245], v[246:247]
	v_mfma_f32_16x16x32_f16 v[52:55], v[56:59], v[140:143], v[52:55]
	v_pk_fma_f32 v[244:245], v[240:241], v[244:245], v[242:243] neg_lo:[1,0,0] neg_hi:[1,0,0]
	v_cvt_pk_f16_f32 v203, v244, v245
	v_mfma_f32_16x16x32_f16 v[48:51], v[64:67], v[140:143], v[48:51]
	v_lshl_add_u64 v[252:253], v[250:251], 0, s[92:93]
	global_store_dwordx4 v[252:253], v[200:203], off offset:256 sc1
	v_mfma_f32_16x16x32_f16 v[20:23], v[56:59], v[148:151], v[20:23]
	v_and_b32_e32 v240, 0x7fffffff, v208
	v_and_b32_e32 v241, 0x7fffffff, v209
	v_mfma_f32_16x16x32_f16 v[16:19], v[64:67], v[148:151], v[16:19]
	v_pk_fma_f32 v[242:243], v[240:241], s[80:81], 1.0 op_sel_hi:[1,0,0]
	v_pk_mul_f32 v[246:247], v[208:209], v[208:209]
	v_mfma_f32_16x16x32_f16 v[4:7], v[56:59], v[156:159], v[4:7]
	v_rcp_f32_e32 v242, v242
	v_rcp_f32_e32 v243, v243
	v_mfma_f32_16x16x32_f16 v[0:3], v[64:67], v[156:159], v[0:3]
	v_pk_mul_f32 v[246:247], v[246:247], s[90:91] op_sel_hi:[1,0]
	v_pk_fma_f32 v[244:245], v[242:243], s[82:83], v[248:249] op_sel_hi:[1,0,1]
	v_mfma_f32_16x16x32_f16 v[68:71], v[64:67], v[96:99], v[68:71]
	v_exp_f32_e32 v246, v246
	v_exp_f32_e32 v247, v247
	s_setprio 0
	s_barrier
	s_mov_b32 m0, s64
	v_lshl_add_u64 v[126:127], v[126:127], 0, s[22:23]
	ds_read_b128 v[44:47], v132
	ds_read_b128 v[56:59], v132 offset:1024
	ds_read_b128 v[60:63], v132 offset:2048
	ds_read_b128 v[64:67], v132 offset:3072
	ds_read_b128 v[80:83], v133
	ds_read_b128 v[96:99], v133 offset:1024
	ds_read_b128 v[136:139], v133 offset:2048
	ds_read_b128 v[140:143], v133 offset:3072
	ds_read_b128 v[144:147], v133 offset:4096
	ds_read_b128 v[148:151], v133 offset:5120
	ds_read_b128 v[152:155], v133 offset:6144
	ds_read_b128 v[156:159], v133 offset:7168
	global_load_lds_dwordx4 v[126:127], off
	v_lshl_add_u64 v[126:127], v[160:161], 0, s[22:23]
	s_mov_b32 m0, s65
	s_add_i32 s46, s76, s54
	global_load_lds_dwordx4 v[126:127], off
	v_lshl_add_u64 v[126:127], v[162:163], 0, s[22:23]
	s_mov_b32 m0, s46
	s_nop 0
	global_load_lds_dwordx4 v[126:127], off
	v_lshl_add_u64 v[126:127], v[164:165], 0, s[22:23]
	s_add_i32 m0, s46, 0x2000
	s_nop 0
	global_load_lds_dwordx4 v[126:127], off
	s_barrier
	s_waitcnt lgkmcnt(0)
	s_setprio 1
	s_waitcnt lgkmcnt(0)
	v_mfma_f32_16x16x32_f16 v[92:95], v[44:47], v[80:83], v[92:95]
	v_pk_fma_f32 v[244:245], v[242:243], v[244:245], s[84:85] op_sel_hi:[1,1,0]
	v_pk_fma_f32 v[244:245], v[242:243], v[244:245], s[86:87] op_sel_hi:[1,1,0]
	v_mfma_f32_16x16x32_f16 v[88:91], v[60:63], v[80:83], v[88:91]
	v_pk_fma_f32 v[244:245], v[242:243], v[244:245], s[88:89] op_sel_hi:[1,1,0]
	v_pk_mul_f32 v[244:245], v[242:243], v[244:245]
	v_mfma_f32_16x16x32_f16 v[76:79], v[44:47], v[136:139], v[76:79]
	v_max_f32_e32 v242, 0, v208
	v_max_f32_e32 v243, 0, v209
	v_mfma_f32_16x16x32_f16 v[72:75], v[60:63], v[136:139], v[72:75]
	v_pk_mul_f32 v[244:245], v[244:245], v[246:247]
	v_pk_fma_f32 v[244:245], v[240:241], v[244:245], v[242:243] neg_lo:[1,0,0] neg_hi:[1,0,0]
	v_mfma_f32_16x16x32_f16 v[28:31], v[44:47], v[144:147], v[28:31]
	v_cvt_pk_f16_f32 v208, v244, v245
	v_and_b32_e32 v240, 0x7fffffff, v210
	v_mfma_f32_16x16x32_f16 v[24:27], v[60:63], v[144:147], v[24:27]
	v_and_b32_e32 v241, 0x7fffffff, v211
	v_pk_fma_f32 v[242:243], v[240:241], s[80:81], 1.0 op_sel_hi:[1,0,0]
	v_mfma_f32_16x16x32_f16 v[12:15], v[44:47], v[152:155], v[12:15]
	v_pk_mul_f32 v[246:247], v[210:211], v[210:211]
	v_rcp_f32_e32 v242, v242
	v_mfma_f32_16x16x32_f16 v[8:11], v[60:63], v[152:155], v[8:11]
	v_rcp_f32_e32 v243, v243
	v_pk_mul_f32 v[246:247], v[246:247], s[90:91] op_sel_hi:[1,0]
	v_mfma_f32_16x16x32_f16 v[92:95], v[56:59], v[96:99], v[92:95]
	v_pk_fma_f32 v[244:245], v[242:243], s[82:83], v[248:249] op_sel_hi:[1,0,1]
	v_exp_f32_e32 v246, v246
	v_mfma_f32_16x16x32_f16 v[88:91], v[64:67], v[96:99], v[88:91]
	v_exp_f32_e32 v247, v247
	v_pk_fma_f32 v[244:245], v[242:243], v[244:245], s[84:85] op_sel_hi:[1,1,0]
	v_mfma_f32_16x16x32_f16 v[76:79], v[56:59], v[140:143], v[76:79]
	v_pk_fma_f32 v[244:245], v[242:243], v[244:245], s[86:87] op_sel_hi:[1,1,0]
	v_pk_fma_f32 v[244:245], v[242:243], v[244:245], s[88:89] op_sel_hi:[1,1,0]
	v_mfma_f32_16x16x32_f16 v[72:75], v[64:67], v[140:143], v[72:75]
	v_pk_mul_f32 v[244:245], v[242:243], v[244:245]
	v_max_f32_e32 v242, 0, v210
	v_mfma_f32_16x16x32_f16 v[28:31], v[56:59], v[148:151], v[28:31]
	v_max_f32_e32 v243, 0, v211
	v_pk_mul_f32 v[244:245], v[244:245], v[246:247]
	v_mfma_f32_16x16x32_f16 v[24:27], v[64:67], v[148:151], v[24:27]
	v_pk_fma_f32 v[244:245], v[240:241], v[244:245], v[242:243] neg_lo:[1,0,0] neg_hi:[1,0,0]
	v_cvt_pk_f16_f32 v209, v244, v245
	v_mfma_f32_16x16x32_f16 v[12:15], v[56:59], v[156:159], v[12:15]
	v_and_b32_e32 v240, 0x7fffffff, v212
	v_and_b32_e32 v241, 0x7fffffff, v213
	v_mfma_f32_16x16x32_f16 v[8:11], v[64:67], v[156:159], v[8:11]
	v_pk_fma_f32 v[242:243], v[240:241], s[80:81], 1.0 op_sel_hi:[1,0,0]
	v_pk_mul_f32 v[246:247], v[212:213], v[212:213]
	s_setprio 0
	s_barrier
	s_add_i32 s46, s48, s54
	v_lshl_add_u64 v[126:127], v[166:167], 0, s[22:23]
	s_mov_b32 m0, s46
	ds_read_b128 v[44:47], v134
	ds_read_b128 v[56:59], v134 offset:1024
	ds_read_b128 v[60:63], v134 offset:2048
	ds_read_b128 v[64:67], v134 offset:3072
	global_load_lds_dwordx4 v[126:127], off
	v_lshl_add_u64 v[126:127], v[168:169], 0, s[22:23]
	s_add_i32 m0, s46, 0x2000
	s_nop 0
	global_load_lds_dwordx4 v[126:127], off
	s_waitcnt vmcnt(7)
	s_barrier
	s_waitcnt lgkmcnt(0)
	s_setprio 1
	s_waitcnt lgkmcnt(0)
	v_mfma_f32_16x16x32_f16 v[84:87], v[44:47], v[80:83], v[84:87]
	v_rcp_f32_e32 v242, v242
	v_rcp_f32_e32 v243, v243
	v_mfma_f32_16x16x32_f16 v[68:71], v[60:63], v[80:83], v[68:71]
	v_pk_mul_f32 v[246:247], v[246:247], s[90:91] op_sel_hi:[1,0]
	v_pk_fma_f32 v[244:245], v[242:243], s[82:83], v[248:249] op_sel_hi:[1,0,1]
	v_mfma_f32_16x16x32_f16 v[52:55], v[44:47], v[136:139], v[52:55]
	v_exp_f32_e32 v246, v246
	v_exp_f32_e32 v247, v247
	v_mfma_f32_16x16x32_f16 v[48:51], v[60:63], v[136:139], v[48:51]
	v_pk_fma_f32 v[244:245], v[242:243], v[244:245], s[84:85] op_sel_hi:[1,1,0]
	v_pk_fma_f32 v[244:245], v[242:243], v[244:245], s[86:87] op_sel_hi:[1,1,0]
	v_mfma_f32_16x16x32_f16 v[20:23], v[44:47], v[144:147], v[20:23]
	v_pk_fma_f32 v[244:245], v[242:243], v[244:245], s[88:89] op_sel_hi:[1,1,0]
	v_pk_mul_f32 v[244:245], v[242:243], v[244:245]
	v_mfma_f32_16x16x32_f16 v[16:19], v[60:63], v[144:147], v[16:19]
	v_max_f32_e32 v242, 0, v212
	v_max_f32_e32 v243, 0, v213
	v_mfma_f32_16x16x32_f16 v[4:7], v[44:47], v[152:155], v[4:7]
	v_pk_mul_f32 v[244:245], v[244:245], v[246:247]
	v_pk_fma_f32 v[244:245], v[240:241], v[244:245], v[242:243] neg_lo:[1,0,0] neg_hi:[1,0,0]
	v_mfma_f32_16x16x32_f16 v[0:3], v[60:63], v[152:155], v[0:3]
	v_cvt_pk_f16_f32 v210, v244, v245
	v_and_b32_e32 v240, 0x7fffffff, v214
	v_mfma_f32_16x16x32_f16 v[84:87], v[56:59], v[96:99], v[84:87]
	v_and_b32_e32 v241, 0x7fffffff, v215
	v_pk_fma_f32 v[242:243], v[240:241], s[80:81], 1.0 op_sel_hi:[1,0,0]
	v_mfma_f32_16x16x32_f16 v[80:83], v[64:67], v[96:99], v[68:71]
	v_pk_mul_f32 v[246:247], v[214:215], v[214:215]
	v_rcp_f32_e32 v242, v242
	v_mfma_f32_16x16x32_f16 v[52:55], v[56:59], v[140:143], v[52:55]
	v_rcp_f32_e32 v243, v243
	v_pk_mul_f32 v[246:247], v[246:247], s[90:91] op_sel_hi:[1,0]
	v_mfma_f32_16x16x32_f16 v[48:51], v[64:67], v[140:143], v[48:51]
	v_pk_fma_f32 v[244:245], v[242:243], s[82:83], v[248:249] op_sel_hi:[1,0,1]
	v_exp_f32_e32 v246, v246
	v_mfma_f32_16x16x32_f16 v[20:23], v[56:59], v[148:151], v[20:23]
	v_exp_f32_e32 v247, v247
	v_pk_fma_f32 v[244:245], v[242:243], v[244:245], s[84:85] op_sel_hi:[1,1,0]
	v_mfma_f32_16x16x32_f16 v[16:19], v[64:67], v[148:151], v[16:19]
	v_pk_fma_f32 v[244:245], v[242:243], v[244:245], s[86:87] op_sel_hi:[1,1,0]
	v_pk_fma_f32 v[244:245], v[242:243], v[244:245], s[88:89] op_sel_hi:[1,1,0]
	v_mfma_f32_16x16x32_f16 v[4:7], v[56:59], v[156:159], v[4:7]
	v_pk_mul_f32 v[244:245], v[242:243], v[244:245]
	v_max_f32_e32 v242, 0, v214
	v_mfma_f32_16x16x32_f16 v[0:3], v[64:67], v[156:159], v[0:3]
	v_max_f32_e32 v243, 0, v215
	v_pk_mul_f32 v[244:245], v[244:245], v[246:247]
	s_setprio 0
	s_barrier
	s_add_i32 s75, s75, 3
	s_add_u32 s44, s44, 0x180
	s_addc_u32 s45, s45, 0
	s_add_u32 s46, s40, s44
	s_addc_u32 s47, s41, s45
	s_add_u32 s46, s46, 0x180
	s_addc_u32 s47, s47, 0
	s_add_u32 s48, s42, s44
	s_addc_u32 s49, s43, s45
	s_add_u32 s76, s48, 0x180
	s_addc_u32 s77, s49, 0
	s_cmp_eq_u32 s67, s75
	s_cselect_b32 s49, s7, s47
	s_cselect_b32 s48, s6, s46
	s_cselect_b32 s47, s5, s77
	s_cselect_b32 s46, s4, s76
	s_add_i32 s76, s19, s54
	v_lshl_add_u64 v[126:127], v[32:33], 0, s[44:45]
	s_mov_b32 m0, s76
	ds_read_b128 v[44:47], v130 offset:16384
	ds_read_b128 v[56:59], v130 offset:17408
	ds_read_b128 v[60:63], v130 offset:18432
	ds_read_b128 v[64:67], v130 offset:19456
	ds_read_b128 v[68:71], v131
	ds_read_b128 v[96:99], v131 offset:1024
	ds_read_b128 v[136:139], v131 offset:2048
	ds_read_b128 v[140:143], v131 offset:3072
	ds_read_b128 v[144:147], v131 offset:4096
	ds_read_b128 v[148:151], v131 offset:5120
	ds_read_b128 v[152:155], v131 offset:6144
	ds_read_b128 v[156:159], v131 offset:7168
	global_load_lds_dwordx4 v[126:127], off
	v_lshl_add_u64 v[126:127], v[34:35], 0, s[44:45]
	s_add_i32 m0, s76, 0x2000
	s_add_i32 s76, s27, s54
	global_load_lds_dwordx4 v[126:127], off
	v_lshl_add_u64 v[126:127], v[36:37], 0, s[44:45]
	s_mov_b32 m0, s76
	s_nop 0
	global_load_lds_dwordx4 v[126:127], off
	v_lshl_add_u64 v[126:127], v[38:39], 0, s[44:45]
	s_add_i32 m0, s76, 0x2000
	s_nop 0
	global_load_lds_dwordx4 v[126:127], off
	s_barrier
	s_waitcnt lgkmcnt(0)
	s_setprio 1
	s_waitcnt lgkmcnt(0)
	v_mfma_f32_16x16x32_f16 v[92:95], v[44:47], v[68:71], v[92:95]
	v_pk_fma_f32 v[244:245], v[240:241], v[244:245], v[242:243] neg_lo:[1,0,0] neg_hi:[1,0,0]
	v_cvt_pk_f16_f32 v211, v244, v245
	v_mfma_f32_16x16x32_f16 v[88:91], v[60:63], v[68:71], v[88:91]
	v_lshl_add_u64 v[252:253], v[250:251], 0, s[94:95]
	global_store_dwordx4 v[252:253], v[208:211], off sc1
	v_mfma_f32_16x16x32_f16 v[76:79], v[44:47], v[136:139], v[76:79]
	v_and_b32_e32 v240, 0x7fffffff, v216
	v_and_b32_e32 v241, 0x7fffffff, v217
	v_mfma_f32_16x16x32_f16 v[72:75], v[60:63], v[136:139], v[72:75]
	v_pk_fma_f32 v[242:243], v[240:241], s[80:81], 1.0 op_sel_hi:[1,0,0]
	v_pk_mul_f32 v[246:247], v[216:217], v[216:217]
	v_mfma_f32_16x16x32_f16 v[28:31], v[44:47], v[144:147], v[28:31]
	v_rcp_f32_e32 v242, v242
	v_rcp_f32_e32 v243, v243
	v_mfma_f32_16x16x32_f16 v[24:27], v[60:63], v[144:147], v[24:27]
	v_pk_mul_f32 v[246:247], v[246:247], s[90:91] op_sel_hi:[1,0]
	v_pk_fma_f32 v[244:245], v[242:243], s[82:83], v[248:249] op_sel_hi:[1,0,1]
	v_mfma_f32_16x16x32_f16 v[12:15], v[44:47], v[152:155], v[12:15]
	v_exp_f32_e32 v246, v246
	v_exp_f32_e32 v247, v247
	v_mfma_f32_16x16x32_f16 v[8:11], v[60:63], v[152:155], v[8:11]
	v_pk_fma_f32 v[244:245], v[242:243], v[244:245], s[84:85] op_sel_hi:[1,1,0]
	v_pk_fma_f32 v[244:245], v[242:243], v[244:245], s[86:87] op_sel_hi:[1,1,0]
	v_mfma_f32_16x16x32_f16 v[92:95], v[56:59], v[96:99], v[92:95]
	v_pk_fma_f32 v[244:245], v[242:243], v[244:245], s[88:89] op_sel_hi:[1,1,0]
	v_pk_mul_f32 v[244:245], v[242:243], v[244:245]
	v_mfma_f32_16x16x32_f16 v[88:91], v[64:67], v[96:99], v[88:91]
	v_max_f32_e32 v242, 0, v216
	v_max_f32_e32 v243, 0, v217
	v_mfma_f32_16x16x32_f16 v[76:79], v[56:59], v[140:143], v[76:79]
	v_pk_mul_f32 v[244:245], v[244:245], v[246:247]
	v_pk_fma_f32 v[244:245], v[240:241], v[244:245], v[242:243] neg_lo:[1,0,0] neg_hi:[1,0,0]
	v_mfma_f32_16x16x32_f16 v[72:75], v[64:67], v[140:143], v[72:75]
	v_cvt_pk_f16_f32 v216, v244, v245
	v_and_b32_e32 v240, 0x7fffffff, v218
	v_mfma_f32_16x16x32_f16 v[28:31], v[56:59], v[148:151], v[28:31]
	v_and_b32_e32 v241, 0x7fffffff, v219
	v_pk_fma_f32 v[242:243], v[240:241], s[80:81], 1.0 op_sel_hi:[1,0,0]
	v_mfma_f32_16x16x32_f16 v[24:27], v[64:67], v[148:151], v[24:27]
	v_pk_mul_f32 v[246:247], v[218:219], v[218:219]
	v_rcp_f32_e32 v242, v242
	v_mfma_f32_16x16x32_f16 v[12:15], v[56:59], v[156:159], v[12:15]
	v_rcp_f32_e32 v243, v243
	v_pk_mul_f32 v[246:247], v[246:247], s[90:91] op_sel_hi:[1,0]
	v_mfma_f32_16x16x32_f16 v[8:11], v[64:67], v[156:159], v[8:11]
	v_pk_fma_f32 v[244:245], v[242:243], s[82:83], v[248:249] op_sel_hi:[1,0,1]
	v_exp_f32_e32 v246, v246
	s_setprio 0
	s_barrier
	s_add_i32 s76, s68, s54
	v_lshl_add_u64 v[126:127], v[40:41], 0, s[44:45]
	s_mov_b32 m0, s76
	ds_read_b128 v[44:47], v130 offset:32768
	ds_read_b128 v[56:59], v130 offset:33792
	ds_read_b128 v[60:63], v130 offset:34816
	ds_read_b128 v[64:67], v130 offset:35840
	global_load_lds_dwordx4 v[126:127], off
	v_lshl_add_u64 v[126:127], v[42:43], 0, s[44:45]
	s_add_i32 m0, s76, 0x2000
	s_nop 0
	global_load_lds_dwordx4 v[126:127], off
	s_waitcnt vmcnt(7)
	s_barrier
	s_waitcnt lgkmcnt(0)
	s_setprio 1
	s_waitcnt lgkmcnt(0)
	v_mfma_f32_16x16x32_f16 v[84:87], v[44:47], v[68:71], v[84:87]
	v_exp_f32_e32 v247, v247
	v_pk_fma_f32 v[244:245], v[242:243], v[244:245], s[84:85] op_sel_hi:[1,1,0]
	v_mfma_f32_16x16x32_f16 v[52:55], v[44:47], v[136:139], v[52:55]
	v_pk_fma_f32 v[244:245], v[242:243], v[244:245], s[86:87] op_sel_hi:[1,1,0]
	v_pk_fma_f32 v[244:245], v[242:243], v[244:245], s[88:89] op_sel_hi:[1,1,0]
	v_mfma_f32_16x16x32_f16 v[48:51], v[60:63], v[136:139], v[48:51]
	v_pk_mul_f32 v[244:245], v[242:243], v[244:245]
	v_max_f32_e32 v242, 0, v218
	v_mfma_f32_16x16x32_f16 v[20:23], v[44:47], v[144:147], v[20:23]
	v_max_f32_e32 v243, 0, v219
	v_pk_mul_f32 v[244:245], v[244:245], v[246:247]
	v_mfma_f32_16x16x32_f16 v[16:19], v[60:63], v[144:147], v[16:19]
	v_pk_fma_f32 v[244:245], v[240:241], v[244:245], v[242:243] neg_lo:[1,0,0] neg_hi:[1,0,0]
	v_cvt_pk_f16_f32 v217, v244, v245
	v_mfma_f32_16x16x32_f16 v[4:7], v[44:47], v[152:155], v[4:7]
	v_and_b32_e32 v240, 0x7fffffff, v220
	v_and_b32_e32 v241, 0x7fffffff, v221
	v_mfma_f32_16x16x32_f16 v[0:3], v[60:63], v[152:155], v[0:3]
	v_pk_fma_f32 v[242:243], v[240:241], s[80:81], 1.0 op_sel_hi:[1,0,0]
	v_pk_mul_f32 v[246:247], v[220:221], v[220:221]
	v_mfma_f32_16x16x32_f16 v[84:87], v[56:59], v[96:99], v[84:87]
	v_rcp_f32_e32 v242, v242
	v_rcp_f32_e32 v243, v243
	v_mfma_f32_16x16x32_f16 v[68:71], v[60:63], v[68:71], v[80:83]
	v_pk_mul_f32 v[246:247], v[246:247], s[90:91] op_sel_hi:[1,0]
	v_pk_fma_f32 v[244:245], v[242:243], s[82:83], v[248:249] op_sel_hi:[1,0,1]
	v_mfma_f32_16x16x32_f16 v[52:55], v[56:59], v[140:143], v[52:55]
	v_exp_f32_e32 v246, v246
	v_exp_f32_e32 v247, v247
	v_mfma_f32_16x16x32_f16 v[48:51], v[64:67], v[140:143], v[48:51]
	v_pk_fma_f32 v[244:245], v[242:243], v[244:245], s[84:85] op_sel_hi:[1,1,0]
	v_pk_fma_f32 v[244:245], v[242:243], v[244:245], s[86:87] op_sel_hi:[1,1,0]
	v_mfma_f32_16x16x32_f16 v[20:23], v[56:59], v[148:151], v[20:23]
	v_pk_fma_f32 v[244:245], v[242:243], v[244:245], s[88:89] op_sel_hi:[1,1,0]
	v_pk_mul_f32 v[244:245], v[242:243], v[244:245]
	v_mfma_f32_16x16x32_f16 v[16:19], v[64:67], v[148:151], v[16:19]
	v_max_f32_e32 v242, 0, v220
	v_max_f32_e32 v243, 0, v221
	v_mfma_f32_16x16x32_f16 v[4:7], v[56:59], v[156:159], v[4:7]
	v_pk_mul_f32 v[244:245], v[244:245], v[246:247]
	v_pk_fma_f32 v[244:245], v[240:241], v[244:245], v[242:243] neg_lo:[1,0,0] neg_hi:[1,0,0]
	v_mfma_f32_16x16x32_f16 v[0:3], v[64:67], v[156:159], v[0:3]
	v_cvt_pk_f16_f32 v218, v244, v245
	v_and_b32_e32 v240, 0x7fffffff, v222
	v_mfma_f32_16x16x32_f16 v[68:71], v[64:67], v[96:99], v[68:71]
	v_and_b32_e32 v241, 0x7fffffff, v223
	v_pk_fma_f32 v[242:243], v[240:241], s[80:81], 1.0 op_sel_hi:[1,0,0]
	s_setprio 0
	s_barrier
	s_add_i32 s76, 0, 0x10000
	s_mov_b32 m0, s57
	v_add_u32_e32 v64, s76, v128
	v_lshl_add_u64 v[126:127], s[48:49], 0, v[100:101]
	ds_read_b128 v[44:47], v64
	ds_read_b128 v[56:59], v64 offset:1024
	ds_read_b128 v[60:63], v64 offset:2048
	ds_read_b128 v[64:67], v64 offset:3072
	ds_read_b128 v[80:83], v131 offset:49152
	ds_read_b128 v[96:99], v131 offset:50176
	ds_read_b128 v[136:139], v131 offset:51200
	ds_read_b128 v[140:143], v131 offset:52224
	ds_read_b128 v[144:147], v131 offset:53248
	ds_read_b128 v[148:151], v131 offset:54272
	ds_read_b128 v[152:155], v131 offset:55296
	ds_read_b128 v[156:159], v131 offset:56320
	global_load_lds_dwordx4 v[126:127], off
	v_lshl_add_u64 v[160:161], s[48:49], 0, v[104:105]
	s_mov_b32 m0, s58
	v_lshl_add_u64 v[162:163], s[46:47], 0, v[102:103]
	global_load_lds_dwordx4 v[160:161], off
	s_mov_b32 m0, s59
	v_lshl_add_u64 v[164:165], s[46:47], 0, v[106:107]
	global_load_lds_dwordx4 v[162:163], off
	s_mov_b32 m0, s60
	s_nop 0
	global_load_lds_dwordx4 v[164:165], off
	s_barrier
	s_waitcnt lgkmcnt(0)
	s_setprio 1
	s_waitcnt lgkmcnt(0)
	v_mfma_f32_16x16x32_f16 v[92:95], v[44:47], v[80:83], v[92:95]
	v_pk_mul_f32 v[246:247], v[222:223], v[222:223]
	v_rcp_f32_e32 v242, v242
	v_mfma_f32_16x16x32_f16 v[88:91], v[60:63], v[80:83], v[88:91]
	v_rcp_f32_e32 v243, v243
	v_pk_mul_f32 v[246:247], v[246:247], s[90:91] op_sel_hi:[1,0]
	v_mfma_f32_16x16x32_f16 v[76:79], v[44:47], v[136:139], v[76:79]
	v_pk_fma_f32 v[244:245], v[242:243], s[82:83], v[248:249] op_sel_hi:[1,0,1]
	v_exp_f32_e32 v246, v246
	v_mfma_f32_16x16x32_f16 v[72:75], v[60:63], v[136:139], v[72:75]
	v_exp_f32_e32 v247, v247
	v_pk_fma_f32 v[244:245], v[242:243], v[244:245], s[84:85] op_sel_hi:[1,1,0]
	v_mfma_f32_16x16x32_f16 v[28:31], v[44:47], v[144:147], v[28:31]
	v_pk_fma_f32 v[244:245], v[242:243], v[244:245], s[86:87] op_sel_hi:[1,1,0]
	v_pk_fma_f32 v[244:245], v[242:243], v[244:245], s[88:89] op_sel_hi:[1,1,0]
	v_mfma_f32_16x16x32_f16 v[24:27], v[60:63], v[144:147], v[24:27]
	v_pk_mul_f32 v[244:245], v[242:243], v[244:245]
	v_max_f32_e32 v242, 0, v222
	v_mfma_f32_16x16x32_f16 v[12:15], v[44:47], v[152:155], v[12:15]
	v_max_f32_e32 v243, 0, v223
	v_pk_mul_f32 v[244:245], v[244:245], v[246:247]
	v_mfma_f32_16x16x32_f16 v[8:11], v[60:63], v[152:155], v[8:11]
	v_pk_fma_f32 v[244:245], v[240:241], v[244:245], v[242:243] neg_lo:[1,0,0] neg_hi:[1,0,0]
	v_cvt_pk_f16_f32 v219, v244, v245
	v_mfma_f32_16x16x32_f16 v[92:95], v[56:59], v[96:99], v[92:95]
	v_lshl_add_u64 v[252:253], v[250:251], 0, s[94:95]
	global_store_dwordx4 v[252:253], v[216:219], off offset:256 sc1
	v_mfma_f32_16x16x32_f16 v[88:91], v[64:67], v[96:99], v[88:91]
	v_and_b32_e32 v240, 0x7fffffff, v224
	v_and_b32_e32 v241, 0x7fffffff, v225
	v_mfma_f32_16x16x32_f16 v[76:79], v[56:59], v[140:143], v[76:79]
	v_pk_fma_f32 v[242:243], v[240:241], s[80:81], 1.0 op_sel_hi:[1,0,0]
	v_pk_mul_f32 v[246:247], v[224:225], v[224:225]
	v_mfma_f32_16x16x32_f16 v[72:75], v[64:67], v[140:143], v[72:75]
	v_rcp_f32_e32 v242, v242
	v_rcp_f32_e32 v243, v243
	v_mfma_f32_16x16x32_f16 v[28:31], v[56:59], v[148:151], v[28:31]
	v_pk_mul_f32 v[246:247], v[246:247], s[90:91] op_sel_hi:[1,0]
	v_pk_fma_f32 v[244:245], v[242:243], s[82:83], v[248:249] op_sel_hi:[1,0,1]
	v_mfma_f32_16x16x32_f16 v[24:27], v[64:67], v[148:151], v[24:27]
	v_exp_f32_e32 v246, v246
	v_exp_f32_e32 v247, v247
	v_mfma_f32_16x16x32_f16 v[12:15], v[56:59], v[156:159], v[12:15]
	v_pk_fma_f32 v[244:245], v[242:243], v[244:245], s[84:85] op_sel_hi:[1,1,0]
	v_pk_fma_f32 v[244:245], v[242:243], v[244:245], s[86:87] op_sel_hi:[1,1,0]
	v_mfma_f32_16x16x32_f16 v[8:11], v[64:67], v[156:159], v[8:11]
	v_pk_fma_f32 v[244:245], v[242:243], v[244:245], s[88:89] op_sel_hi:[1,1,0]
	v_pk_mul_f32 v[244:245], v[242:243], v[244:245]
	s_setprio 0
	s_barrier
	s_add_i32 s48, 0, 0x14000
	s_add_u32 s46, s46, s10
	s_addc_u32 s47, s47, s11
	s_mov_b32 m0, s61
	v_add_u32_e32 v64, s48, v128
	v_lshl_add_u64 v[166:167], s[46:47], 0, v[102:103]
	ds_read_b128 v[44:47], v64
	ds_read_b128 v[56:59], v64 offset:1024
	ds_read_b128 v[60:63], v64 offset:2048
	ds_read_b128 v[64:67], v64 offset:3072
	global_load_lds_dwordx4 v[166:167], off
	v_lshl_add_u64 v[168:169], s[46:47], 0, v[106:107]
	s_mov_b32 m0, s62
	s_nop 0
	global_load_lds_dwordx4 v[168:169], off
	s_waitcnt vmcnt(7)
	s_barrier
	s_waitcnt lgkmcnt(0)
	s_setprio 1
	s_waitcnt lgkmcnt(0)
	v_mfma_f32_16x16x32_f16 v[84:87], v[44:47], v[80:83], v[84:87]
	v_max_f32_e32 v242, 0, v224
	v_max_f32_e32 v243, 0, v225
	v_mfma_f32_16x16x32_f16 v[52:55], v[44:47], v[136:139], v[52:55]
	v_pk_mul_f32 v[244:245], v[244:245], v[246:247]
	v_pk_fma_f32 v[244:245], v[240:241], v[244:245], v[242:243] neg_lo:[1,0,0] neg_hi:[1,0,0]
	v_mfma_f32_16x16x32_f16 v[48:51], v[60:63], v[136:139], v[48:51]
	v_cvt_pk_f16_f32 v224, v244, v245
	v_and_b32_e32 v240, 0x7fffffff, v226
	v_mfma_f32_16x16x32_f16 v[20:23], v[44:47], v[144:147], v[20:23]
	v_and_b32_e32 v241, 0x7fffffff, v227
	v_pk_fma_f32 v[242:243], v[240:241], s[80:81], 1.0 op_sel_hi:[1,0,0]
	v_mfma_f32_16x16x32_f16 v[16:19], v[60:63], v[144:147], v[16:19]
	v_pk_mul_f32 v[246:247], v[226:227], v[226:227]
	v_rcp_f32_e32 v242, v242
	v_mfma_f32_16x16x32_f16 v[4:7], v[44:47], v[152:155], v[4:7]
	v_rcp_f32_e32 v243, v243
	v_pk_mul_f32 v[246:247], v[246:247], s[90:91] op_sel_hi:[1,0]
	v_mfma_f32_16x16x32_f16 v[0:3], v[60:63], v[152:155], v[0:3]
	v_pk_fma_f32 v[244:245], v[242:243], s[82:83], v[248:249] op_sel_hi:[1,0,1]
	v_exp_f32_e32 v246, v246
	v_mfma_f32_16x16x32_f16 v[84:87], v[56:59], v[96:99], v[84:87]
	v_exp_f32_e32 v247, v247
	v_pk_fma_f32 v[244:245], v[242:243], v[244:245], s[84:85] op_sel_hi:[1,1,0]
	v_mfma_f32_16x16x32_f16 v[68:71], v[60:63], v[80:83], v[68:71]
	v_pk_fma_f32 v[244:245], v[242:243], v[244:245], s[86:87] op_sel_hi:[1,1,0]
	v_pk_fma_f32 v[244:245], v[242:243], v[244:245], s[88:89] op_sel_hi:[1,1,0]
	v_mfma_f32_16x16x32_f16 v[52:55], v[56:59], v[140:143], v[52:55]
	v_pk_mul_f32 v[244:245], v[242:243], v[244:245]
	v_max_f32_e32 v242, 0, v226
	v_mfma_f32_16x16x32_f16 v[48:51], v[64:67], v[140:143], v[48:51]
	v_max_f32_e32 v243, 0, v227
	v_pk_mul_f32 v[244:245], v[244:245], v[246:247]
	v_mfma_f32_16x16x32_f16 v[20:23], v[56:59], v[148:151], v[20:23]
	v_pk_fma_f32 v[244:245], v[240:241], v[244:245], v[242:243] neg_lo:[1,0,0] neg_hi:[1,0,0]
	v_cvt_pk_f16_f32 v225, v244, v245
	v_mfma_f32_16x16x32_f16 v[16:19], v[64:67], v[148:151], v[16:19]
	v_and_b32_e32 v240, 0x7fffffff, v228
	v_and_b32_e32 v241, 0x7fffffff, v229
	v_mfma_f32_16x16x32_f16 v[4:7], v[56:59], v[156:159], v[4:7]
	v_pk_fma_f32 v[242:243], v[240:241], s[80:81], 1.0 op_sel_hi:[1,0,0]
	v_pk_mul_f32 v[246:247], v[228:229], v[228:229]
	v_mfma_f32_16x16x32_f16 v[0:3], v[64:67], v[156:159], v[0:3]
	v_rcp_f32_e32 v242, v242
	v_rcp_f32_e32 v243, v243
	v_mfma_f32_16x16x32_f16 v[68:71], v[64:67], v[96:99], v[68:71]
	v_pk_mul_f32 v[246:247], v[246:247], s[90:91] op_sel_hi:[1,0]
	v_pk_fma_f32 v[244:245], v[242:243], s[82:83], v[248:249] op_sel_hi:[1,0,1]
	s_setprio 0
	s_barrier
	s_mov_b32 m0, s64
	v_lshl_add_u64 v[126:127], v[126:127], 0, s[22:23]
	ds_read_b128 v[44:47], v132
	ds_read_b128 v[56:59], v132 offset:1024
	ds_read_b128 v[60:63], v132 offset:2048
	ds_read_b128 v[64:67], v132 offset:3072
	ds_read_b128 v[80:83], v133
	ds_read_b128 v[96:99], v133 offset:1024
	ds_read_b128 v[136:139], v133 offset:2048
	ds_read_b128 v[140:143], v133 offset:3072
	ds_read_b128 v[144:147], v133 offset:4096
	ds_read_b128 v[148:151], v133 offset:5120
	ds_read_b128 v[152:155], v133 offset:6144
	ds_read_b128 v[156:159], v133 offset:7168
	global_load_lds_dwordx4 v[126:127], off
	v_lshl_add_u64 v[126:127], v[160:161], 0, s[22:23]
	s_mov_b32 m0, s65
	s_add_i32 s46, s76, s54
	global_load_lds_dwordx4 v[126:127], off
	v_lshl_add_u64 v[126:127], v[162:163], 0, s[22:23]
	s_mov_b32 m0, s46
	s_nop 0
	global_load_lds_dwordx4 v[126:127], off
	v_lshl_add_u64 v[126:127], v[164:165], 0, s[22:23]
	s_add_i32 m0, s46, 0x2000
	s_nop 0
	global_load_lds_dwordx4 v[126:127], off
	s_barrier
	s_waitcnt lgkmcnt(0)
	s_setprio 1
	s_waitcnt lgkmcnt(0)
	v_mfma_f32_16x16x32_f16 v[92:95], v[44:47], v[80:83], v[92:95]
	v_exp_f32_e32 v246, v246
	v_exp_f32_e32 v247, v247
	v_mfma_f32_16x16x32_f16 v[88:91], v[60:63], v[80:83], v[88:91]
	v_pk_fma_f32 v[244:245], v[242:243], v[244:245], s[84:85] op_sel_hi:[1,1,0]
	v_pk_fma_f32 v[244:245], v[242:243], v[244:245], s[86:87] op_sel_hi:[1,1,0]
	v_mfma_f32_16x16x32_f16 v[76:79], v[44:47], v[136:139], v[76:79]
	v_pk_fma_f32 v[244:245], v[242:243], v[244:245], s[88:89] op_sel_hi:[1,1,0]
	v_pk_mul_f32 v[244:245], v[242:243], v[244:245]
	v_mfma_f32_16x16x32_f16 v[72:75], v[60:63], v[136:139], v[72:75]
	v_max_f32_e32 v242, 0, v228
	v_max_f32_e32 v243, 0, v229
	v_mfma_f32_16x16x32_f16 v[28:31], v[44:47], v[144:147], v[28:31]
	v_pk_mul_f32 v[244:245], v[244:245], v[246:247]
	v_pk_fma_f32 v[244:245], v[240:241], v[244:245], v[242:243] neg_lo:[1,0,0] neg_hi:[1,0,0]
	v_mfma_f32_16x16x32_f16 v[24:27], v[60:63], v[144:147], v[24:27]
	v_cvt_pk_f16_f32 v226, v244, v245
	v_and_b32_e32 v240, 0x7fffffff, v230
	v_mfma_f32_16x16x32_f16 v[12:15], v[44:47], v[152:155], v[12:15]
	v_and_b32_e32 v241, 0x7fffffff, v231
	v_pk_fma_f32 v[242:243], v[240:241], s[80:81], 1.0 op_sel_hi:[1,0,0]
	v_mfma_f32_16x16x32_f16 v[8:11], v[60:63], v[152:155], v[8:11]
	v_pk_mul_f32 v[246:247], v[230:231], v[230:231]
	v_rcp_f32_e32 v242, v242
	v_mfma_f32_16x16x32_f16 v[92:95], v[56:59], v[96:99], v[92:95]
	v_rcp_f32_e32 v243, v243
	v_pk_mul_f32 v[246:247], v[246:247], s[90:91] op_sel_hi:[1,0]
	v_mfma_f32_16x16x32_f16 v[88:91], v[64:67], v[96:99], v[88:91]
	v_pk_fma_f32 v[244:245], v[242:243], s[82:83], v[248:249] op_sel_hi:[1,0,1]
	v_exp_f32_e32 v246, v246
	v_mfma_f32_16x16x32_f16 v[76:79], v[56:59], v[140:143], v[76:79]
	v_exp_f32_e32 v247, v247
	v_pk_fma_f32 v[244:245], v[242:243], v[244:245], s[84:85] op_sel_hi:[1,1,0]
	v_mfma_f32_16x16x32_f16 v[72:75], v[64:67], v[140:143], v[72:75]
	v_pk_fma_f32 v[244:245], v[242:243], v[244:245], s[86:87] op_sel_hi:[1,1,0]
	v_pk_fma_f32 v[244:245], v[242:243], v[244:245], s[88:89] op_sel_hi:[1,1,0]
	v_mfma_f32_16x16x32_f16 v[28:31], v[56:59], v[148:151], v[28:31]
	v_pk_mul_f32 v[244:245], v[242:243], v[244:245]
	v_max_f32_e32 v242, 0, v230
	v_mfma_f32_16x16x32_f16 v[24:27], v[64:67], v[148:151], v[24:27]
	v_max_f32_e32 v243, 0, v231
	v_pk_mul_f32 v[244:245], v[244:245], v[246:247]
	v_mfma_f32_16x16x32_f16 v[12:15], v[56:59], v[156:159], v[12:15]
	v_pk_fma_f32 v[244:245], v[240:241], v[244:245], v[242:243] neg_lo:[1,0,0] neg_hi:[1,0,0]
	v_cvt_pk_f16_f32 v227, v244, v245
	v_mfma_f32_16x16x32_f16 v[8:11], v[64:67], v[156:159], v[8:11]
	v_lshl_add_u64 v[252:253], v[250:251], 0, s[96:97]
	global_store_dwordx4 v[252:253], v[224:227], off sc1
	s_setprio 0
	s_barrier
	s_add_i32 s46, s48, s54
	v_lshl_add_u64 v[126:127], v[166:167], 0, s[22:23]
	s_mov_b32 m0, s46
	ds_read_b128 v[44:47], v134
	ds_read_b128 v[56:59], v134 offset:1024
	ds_read_b128 v[60:63], v134 offset:2048
	ds_read_b128 v[64:67], v134 offset:3072
	global_load_lds_dwordx4 v[126:127], off
	v_lshl_add_u64 v[126:127], v[168:169], 0, s[22:23]
	s_add_i32 m0, s46, 0x2000
	s_nop 0
	global_load_lds_dwordx4 v[126:127], off
	s_waitcnt vmcnt(7)
	s_barrier
	s_waitcnt lgkmcnt(0)
	s_setprio 1
	s_waitcnt lgkmcnt(0)
	v_mfma_f32_16x16x32_f16 v[84:87], v[44:47], v[80:83], v[84:87]
	v_and_b32_e32 v240, 0x7fffffff, v232
	v_and_b32_e32 v241, 0x7fffffff, v233
	v_mfma_f32_16x16x32_f16 v[68:71], v[60:63], v[80:83], v[68:71]
	v_pk_fma_f32 v[242:243], v[240:241], s[80:81], 1.0 op_sel_hi:[1,0,0]
	v_pk_mul_f32 v[246:247], v[232:233], v[232:233]
	v_mfma_f32_16x16x32_f16 v[52:55], v[44:47], v[136:139], v[52:55]
	v_rcp_f32_e32 v242, v242
	v_rcp_f32_e32 v243, v243
	v_mfma_f32_16x16x32_f16 v[48:51], v[60:63], v[136:139], v[48:51]
	v_pk_mul_f32 v[246:247], v[246:247], s[90:91] op_sel_hi:[1,0]
	v_pk_fma_f32 v[244:245], v[242:243], s[82:83], v[248:249] op_sel_hi:[1,0,1]
	v_mfma_f32_16x16x32_f16 v[20:23], v[44:47], v[144:147], v[20:23]
	v_exp_f32_e32 v246, v246
	v_exp_f32_e32 v247, v247
	v_mfma_f32_16x16x32_f16 v[16:19], v[60:63], v[144:147], v[16:19]
	v_pk_fma_f32 v[244:245], v[242:243], v[244:245], s[84:85] op_sel_hi:[1,1,0]
	v_pk_fma_f32 v[244:245], v[242:243], v[244:245], s[86:87] op_sel_hi:[1,1,0]
	v_mfma_f32_16x16x32_f16 v[4:7], v[44:47], v[152:155], v[4:7]
	v_pk_fma_f32 v[244:245], v[242:243], v[244:245], s[88:89] op_sel_hi:[1,1,0]
	v_pk_mul_f32 v[244:245], v[242:243], v[244:245]
	v_mfma_f32_16x16x32_f16 v[0:3], v[60:63], v[152:155], v[0:3]
	v_max_f32_e32 v242, 0, v232
	v_max_f32_e32 v243, 0, v233
	v_mfma_f32_16x16x32_f16 v[84:87], v[56:59], v[96:99], v[84:87]
	v_pk_mul_f32 v[244:245], v[244:245], v[246:247]
	v_pk_fma_f32 v[244:245], v[240:241], v[244:245], v[242:243] neg_lo:[1,0,0] neg_hi:[1,0,0]
	v_mfma_f32_16x16x32_f16 v[80:83], v[64:67], v[96:99], v[68:71]
	v_cvt_pk_f16_f32 v232, v244, v245
	v_and_b32_e32 v240, 0x7fffffff, v234
	v_mfma_f32_16x16x32_f16 v[52:55], v[56:59], v[140:143], v[52:55]
	v_and_b32_e32 v241, 0x7fffffff, v235
	v_pk_fma_f32 v[242:243], v[240:241], s[80:81], 1.0 op_sel_hi:[1,0,0]
	v_mfma_f32_16x16x32_f16 v[48:51], v[64:67], v[140:143], v[48:51]
	v_pk_mul_f32 v[246:247], v[234:235], v[234:235]
	v_rcp_f32_e32 v242, v242
	v_mfma_f32_16x16x32_f16 v[20:23], v[56:59], v[148:151], v[20:23]
	v_rcp_f32_e32 v243, v243
	v_pk_mul_f32 v[246:247], v[246:247], s[90:91] op_sel_hi:[1,0]
	v_mfma_f32_16x16x32_f16 v[16:19], v[64:67], v[148:151], v[16:19]
	v_pk_fma_f32 v[244:245], v[242:243], s[82:83], v[248:249] op_sel_hi:[1,0,1]
	v_exp_f32_e32 v246, v246
	v_mfma_f32_16x16x32_f16 v[4:7], v[56:59], v[156:159], v[4:7]
	v_exp_f32_e32 v247, v247
	v_pk_fma_f32 v[244:245], v[242:243], v[244:245], s[84:85] op_sel_hi:[1,1,0]
	v_mfma_f32_16x16x32_f16 v[0:3], v[64:67], v[156:159], v[0:3]
	v_pk_fma_f32 v[244:245], v[242:243], v[244:245], s[86:87] op_sel_hi:[1,1,0]
	v_pk_fma_f32 v[244:245], v[242:243], v[244:245], s[88:89] op_sel_hi:[1,1,0]
	s_setprio 0
	s_barrier
	s_add_i32 s75, s75, 3
	s_add_u32 s44, s44, 0x180
	s_addc_u32 s45, s45, 0
	s_add_u32 s46, s40, s44
	s_addc_u32 s47, s41, s45
	s_add_u32 s46, s46, 0x180
	s_addc_u32 s47, s47, 0
	s_add_u32 s48, s42, s44
	s_addc_u32 s49, s43, s45
	s_add_u32 s76, s48, 0x180
	s_addc_u32 s77, s49, 0
	s_cmp_eq_u32 s67, s75
	s_cselect_b32 s49, s7, s47
	s_cselect_b32 s48, s6, s46
	s_cselect_b32 s47, s5, s77
	s_cselect_b32 s46, s4, s76
	s_add_i32 s76, s19, s54
	v_lshl_add_u64 v[126:127], v[32:33], 0, s[44:45]
	s_mov_b32 m0, s76
	ds_read_b128 v[44:47], v130 offset:16384
	ds_read_b128 v[56:59], v130 offset:17408
	ds_read_b128 v[60:63], v130 offset:18432
	ds_read_b128 v[64:67], v130 offset:19456
	ds_read_b128 v[68:71], v131
	ds_read_b128 v[96:99], v131 offset:1024
	ds_read_b128 v[136:139], v131 offset:2048
	ds_read_b128 v[140:143], v131 offset:3072
	ds_read_b128 v[144:147], v131 offset:4096
	ds_read_b128 v[148:151], v131 offset:5120
	ds_read_b128 v[152:155], v131 offset:6144
	ds_read_b128 v[156:159], v131 offset:7168
	global_load_lds_dwordx4 v[126:127], off
	v_lshl_add_u64 v[126:127], v[34:35], 0, s[44:45]
	s_add_i32 m0, s76, 0x2000
	s_add_i32 s76, s27, s54
	global_load_lds_dwordx4 v[126:127], off
	v_lshl_add_u64 v[126:127], v[36:37], 0, s[44:45]
	s_mov_b32 m0, s76
	s_nop 0
	global_load_lds_dwordx4 v[126:127], off
	v_lshl_add_u64 v[126:127], v[38:39], 0, s[44:45]
	s_add_i32 m0, s76, 0x2000
	s_nop 0
	global_load_lds_dwordx4 v[126:127], off
	s_barrier
	s_waitcnt lgkmcnt(0)
	s_setprio 1
	s_waitcnt lgkmcnt(0)
	v_mfma_f32_16x16x32_f16 v[92:95], v[44:47], v[68:71], v[92:95]
	v_pk_mul_f32 v[244:245], v[242:243], v[244:245]
	v_max_f32_e32 v242, 0, v234
	v_mfma_f32_16x16x32_f16 v[88:91], v[60:63], v[68:71], v[88:91]
	v_max_f32_e32 v243, 0, v235
	v_pk_mul_f32 v[244:245], v[244:245], v[246:247]
	v_mfma_f32_16x16x32_f16 v[76:79], v[44:47], v[136:139], v[76:79]
	v_pk_fma_f32 v[244:245], v[240:241], v[244:245], v[242:243] neg_lo:[1,0,0] neg_hi:[1,0,0]
	v_cvt_pk_f16_f32 v233, v244, v245
	v_mfma_f32_16x16x32_f16 v[72:75], v[60:63], v[136:139], v[72:75]
	v_and_b32_e32 v240, 0x7fffffff, v236
	v_and_b32_e32 v241, 0x7fffffff, v237
	v_mfma_f32_16x16x32_f16 v[28:31], v[44:47], v[144:147], v[28:31]
	v_pk_fma_f32 v[242:243], v[240:241], s[80:81], 1.0 op_sel_hi:[1,0,0]
	v_pk_mul_f32 v[246:247], v[236:237], v[236:237]
	v_mfma_f32_16x16x32_f16 v[24:27], v[60:63], v[144:147], v[24:27]
	v_rcp_f32_e32 v242, v242
	v_rcp_f32_e32 v243, v243
	v_mfma_f32_16x16x32_f16 v[12:15], v[44:47], v[152:155], v[12:15]
	v_pk_mul_f32 v[246:247], v[246:247], s[90:91] op_sel_hi:[1,0]
	v_pk_fma_f32 v[244:245], v[242:243], s[82:83], v[248:249] op_sel_hi:[1,0,1]
	v_mfma_f32_16x16x32_f16 v[8:11], v[60:63], v[152:155], v[8:11]
	v_exp_f32_e32 v246, v246
	v_exp_f32_e32 v247, v247
	v_mfma_f32_16x16x32_f16 v[92:95], v[56:59], v[96:99], v[92:95]
	v_pk_fma_f32 v[244:245], v[242:243], v[244:245], s[84:85] op_sel_hi:[1,1,0]
	v_pk_fma_f32 v[244:245], v[242:243], v[244:245], s[86:87] op_sel_hi:[1,1,0]
	v_mfma_f32_16x16x32_f16 v[88:91], v[64:67], v[96:99], v[88:91]
	v_pk_fma_f32 v[244:245], v[242:243], v[244:245], s[88:89] op_sel_hi:[1,1,0]
	v_pk_mul_f32 v[244:245], v[242:243], v[244:245]
	v_mfma_f32_16x16x32_f16 v[76:79], v[56:59], v[140:143], v[76:79]
	v_max_f32_e32 v242, 0, v236
	v_max_f32_e32 v243, 0, v237
	v_mfma_f32_16x16x32_f16 v[72:75], v[64:67], v[140:143], v[72:75]
	v_pk_mul_f32 v[244:245], v[244:245], v[246:247]
	v_pk_fma_f32 v[244:245], v[240:241], v[244:245], v[242:243] neg_lo:[1,0,0] neg_hi:[1,0,0]
	v_mfma_f32_16x16x32_f16 v[28:31], v[56:59], v[148:151], v[28:31]
	v_cvt_pk_f16_f32 v234, v244, v245
	v_and_b32_e32 v240, 0x7fffffff, v238
	v_mfma_f32_16x16x32_f16 v[24:27], v[64:67], v[148:151], v[24:27]
	v_and_b32_e32 v241, 0x7fffffff, v239
	v_pk_fma_f32 v[242:243], v[240:241], s[80:81], 1.0 op_sel_hi:[1,0,0]
	v_mfma_f32_16x16x32_f16 v[12:15], v[56:59], v[156:159], v[12:15]
	v_pk_mul_f32 v[246:247], v[238:239], v[238:239]
	v_rcp_f32_e32 v242, v242
	v_mfma_f32_16x16x32_f16 v[8:11], v[64:67], v[156:159], v[8:11]
	v_rcp_f32_e32 v243, v243
	v_pk_mul_f32 v[246:247], v[246:247], s[90:91] op_sel_hi:[1,0]
	s_setprio 0
	s_barrier
	s_add_i32 s76, s68, s54
	v_lshl_add_u64 v[126:127], v[40:41], 0, s[44:45]
	s_mov_b32 m0, s76
	ds_read_b128 v[44:47], v130 offset:32768
	ds_read_b128 v[56:59], v130 offset:33792
	ds_read_b128 v[60:63], v130 offset:34816
	ds_read_b128 v[64:67], v130 offset:35840
	global_load_lds_dwordx4 v[126:127], off
	v_lshl_add_u64 v[126:127], v[42:43], 0, s[44:45]
	s_add_i32 m0, s76, 0x2000
	s_nop 0
	global_load_lds_dwordx4 v[126:127], off
	s_waitcnt vmcnt(6)
	s_barrier
	s_waitcnt lgkmcnt(0)
	s_setprio 1
	s_waitcnt lgkmcnt(0)
	v_mfma_f32_16x16x32_f16 v[84:87], v[44:47], v[68:71], v[84:87]
	v_pk_fma_f32 v[244:245], v[242:243], s[82:83], v[248:249] op_sel_hi:[1,0,1]
	v_exp_f32_e32 v246, v246
	v_mfma_f32_16x16x32_f16 v[52:55], v[44:47], v[136:139], v[52:55]
	v_exp_f32_e32 v247, v247
	v_pk_fma_f32 v[244:245], v[242:243], v[244:245], s[84:85] op_sel_hi:[1,1,0]
	v_mfma_f32_16x16x32_f16 v[48:51], v[60:63], v[136:139], v[48:51]
	v_pk_fma_f32 v[244:245], v[242:243], v[244:245], s[86:87] op_sel_hi:[1,1,0]
	v_pk_fma_f32 v[244:245], v[242:243], v[244:245], s[88:89] op_sel_hi:[1,1,0]
	v_mfma_f32_16x16x32_f16 v[20:23], v[44:47], v[144:147], v[20:23]
	v_pk_mul_f32 v[244:245], v[242:243], v[244:245]
	v_max_f32_e32 v242, 0, v238
	v_mfma_f32_16x16x32_f16 v[16:19], v[60:63], v[144:147], v[16:19]
	v_max_f32_e32 v243, 0, v239
	v_pk_mul_f32 v[244:245], v[244:245], v[246:247]
	v_mfma_f32_16x16x32_f16 v[4:7], v[44:47], v[152:155], v[4:7]
	v_pk_fma_f32 v[244:245], v[240:241], v[244:245], v[242:243] neg_lo:[1,0,0] neg_hi:[1,0,0]
	v_cvt_pk_f16_f32 v235, v244, v245
	v_mfma_f32_16x16x32_f16 v[0:3], v[60:63], v[152:155], v[0:3]
	v_lshl_add_u64 v[252:253], v[250:251], 0, s[96:97]
	global_store_dwordx4 v[252:253], v[232:235], off offset:256 sc1
	v_mfma_f32_16x16x32_f16 v[84:87], v[56:59], v[96:99], v[84:87]
	v_mfma_f32_16x16x32_f16 v[68:71], v[60:63], v[68:71], v[80:83]
	v_mfma_f32_16x16x32_f16 v[52:55], v[56:59], v[140:143], v[52:55]
	v_mfma_f32_16x16x32_f16 v[48:51], v[64:67], v[140:143], v[48:51]
	v_mfma_f32_16x16x32_f16 v[20:23], v[56:59], v[148:151], v[20:23]
	v_mfma_f32_16x16x32_f16 v[16:19], v[64:67], v[148:151], v[16:19]
	v_mfma_f32_16x16x32_f16 v[4:7], v[56:59], v[156:159], v[4:7]
	v_mfma_f32_16x16x32_f16 v[0:3], v[64:67], v[156:159], v[0:3]
	v_mfma_f32_16x16x32_f16 v[68:71], v[64:67], v[96:99], v[68:71]
	s_setprio 0
	s_barrier
	s_add_i32 s76, 0, 0x10000
	s_mov_b32 m0, s57
	v_add_u32_e32 v64, s76, v128
	v_lshl_add_u64 v[126:127], s[48:49], 0, v[100:101]
	ds_read_b128 v[44:47], v64
	ds_read_b128 v[56:59], v64 offset:1024
	ds_read_b128 v[60:63], v64 offset:2048
	ds_read_b128 v[64:67], v64 offset:3072
	ds_read_b128 v[80:83], v131 offset:49152
	ds_read_b128 v[96:99], v131 offset:50176
	ds_read_b128 v[136:139], v131 offset:51200
	ds_read_b128 v[140:143], v131 offset:52224
	ds_read_b128 v[144:147], v131 offset:53248
	ds_read_b128 v[148:151], v131 offset:54272
	ds_read_b128 v[152:155], v131 offset:55296
	ds_read_b128 v[156:159], v131 offset:56320
	global_load_lds_dwordx4 v[126:127], off
	v_lshl_add_u64 v[160:161], s[48:49], 0, v[104:105]
	s_mov_b32 m0, s58
	v_lshl_add_u64 v[162:163], s[46:47], 0, v[102:103]
	global_load_lds_dwordx4 v[160:161], off
	s_mov_b32 m0, s59
	v_lshl_add_u64 v[164:165], s[46:47], 0, v[106:107]
	global_load_lds_dwordx4 v[162:163], off
	s_mov_b32 m0, s60
	s_nop 0
	global_load_lds_dwordx4 v[164:165], off
	s_barrier
	s_waitcnt lgkmcnt(0)
	s_setprio 1
	s_waitcnt lgkmcnt(0)
	v_mfma_f32_16x16x32_f16 v[92:95], v[44:47], v[80:83], v[92:95]
	v_mfma_f32_16x16x32_f16 v[88:91], v[60:63], v[80:83], v[88:91]
	v_mfma_f32_16x16x32_f16 v[76:79], v[44:47], v[136:139], v[76:79]
	v_mfma_f32_16x16x32_f16 v[72:75], v[60:63], v[136:139], v[72:75]
	v_mfma_f32_16x16x32_f16 v[28:31], v[44:47], v[144:147], v[28:31]
	v_mfma_f32_16x16x32_f16 v[24:27], v[60:63], v[144:147], v[24:27]
	v_mfma_f32_16x16x32_f16 v[12:15], v[44:47], v[152:155], v[12:15]
	v_mfma_f32_16x16x32_f16 v[8:11], v[60:63], v[152:155], v[8:11]
	v_mfma_f32_16x16x32_f16 v[92:95], v[56:59], v[96:99], v[92:95]
	v_mfma_f32_16x16x32_f16 v[88:91], v[64:67], v[96:99], v[88:91]
	v_mfma_f32_16x16x32_f16 v[76:79], v[56:59], v[140:143], v[76:79]
	v_mfma_f32_16x16x32_f16 v[72:75], v[64:67], v[140:143], v[72:75]
	v_mfma_f32_16x16x32_f16 v[28:31], v[56:59], v[148:151], v[28:31]
	v_mfma_f32_16x16x32_f16 v[24:27], v[64:67], v[148:151], v[24:27]
	v_mfma_f32_16x16x32_f16 v[12:15], v[56:59], v[156:159], v[12:15]
	v_mfma_f32_16x16x32_f16 v[8:11], v[64:67], v[156:159], v[8:11]
	s_setprio 0
	s_barrier
	s_add_i32 s48, 0, 0x14000
	s_add_u32 s46, s46, s10
	s_addc_u32 s47, s47, s11
	s_mov_b32 m0, s61
	v_add_u32_e32 v64, s48, v128
	v_lshl_add_u64 v[166:167], s[46:47], 0, v[102:103]
	ds_read_b128 v[44:47], v64
	ds_read_b128 v[56:59], v64 offset:1024
	ds_read_b128 v[60:63], v64 offset:2048
	ds_read_b128 v[64:67], v64 offset:3072
	global_load_lds_dwordx4 v[166:167], off
	v_lshl_add_u64 v[168:169], s[46:47], 0, v[106:107]
	s_mov_b32 m0, s62
	s_nop 0
	global_load_lds_dwordx4 v[168:169], off
	s_waitcnt vmcnt(7)
	s_barrier
	s_waitcnt lgkmcnt(0)
	s_setprio 1
	s_waitcnt lgkmcnt(0)
	v_mfma_f32_16x16x32_f16 v[84:87], v[44:47], v[80:83], v[84:87]
	v_mfma_f32_16x16x32_f16 v[52:55], v[44:47], v[136:139], v[52:55]
	v_mfma_f32_16x16x32_f16 v[48:51], v[60:63], v[136:139], v[48:51]
	v_mfma_f32_16x16x32_f16 v[20:23], v[44:47], v[144:147], v[20:23]
	v_mfma_f32_16x16x32_f16 v[16:19], v[60:63], v[144:147], v[16:19]
	v_mfma_f32_16x16x32_f16 v[4:7], v[44:47], v[152:155], v[4:7]
	v_mfma_f32_16x16x32_f16 v[0:3], v[60:63], v[152:155], v[0:3]
	v_mfma_f32_16x16x32_f16 v[84:87], v[56:59], v[96:99], v[84:87]
	v_mfma_f32_16x16x32_f16 v[68:71], v[60:63], v[80:83], v[68:71]
	v_mfma_f32_16x16x32_f16 v[52:55], v[56:59], v[140:143], v[52:55]
	v_mfma_f32_16x16x32_f16 v[48:51], v[64:67], v[140:143], v[48:51]
	v_mfma_f32_16x16x32_f16 v[20:23], v[56:59], v[148:151], v[20:23]
	v_mfma_f32_16x16x32_f16 v[16:19], v[64:67], v[148:151], v[16:19]
	v_mfma_f32_16x16x32_f16 v[4:7], v[56:59], v[156:159], v[4:7]
	v_mfma_f32_16x16x32_f16 v[0:3], v[64:67], v[156:159], v[0:3]
	v_mfma_f32_16x16x32_f16 v[68:71], v[64:67], v[96:99], v[68:71]
	s_setprio 0
	s_barrier
	s_mov_b32 m0, s64
	v_lshl_add_u64 v[126:127], v[126:127], 0, s[22:23]
	ds_read_b128 v[44:47], v132
	ds_read_b128 v[56:59], v132 offset:1024
	ds_read_b128 v[60:63], v132 offset:2048
	ds_read_b128 v[64:67], v132 offset:3072
	ds_read_b128 v[80:83], v133
	ds_read_b128 v[96:99], v133 offset:1024
	ds_read_b128 v[136:139], v133 offset:2048
	ds_read_b128 v[140:143], v133 offset:3072
	ds_read_b128 v[144:147], v133 offset:4096
	ds_read_b128 v[148:151], v133 offset:5120
	ds_read_b128 v[152:155], v133 offset:6144
	ds_read_b128 v[156:159], v133 offset:7168
	global_load_lds_dwordx4 v[126:127], off
	v_lshl_add_u64 v[126:127], v[160:161], 0, s[22:23]
	s_mov_b32 m0, s65
	s_add_i32 s46, s76, s54
	global_load_lds_dwordx4 v[126:127], off
	v_lshl_add_u64 v[126:127], v[162:163], 0, s[22:23]
	s_mov_b32 m0, s46
	s_nop 0
	global_load_lds_dwordx4 v[126:127], off
	v_lshl_add_u64 v[126:127], v[164:165], 0, s[22:23]
	s_add_i32 m0, s46, 0x2000
	s_nop 0
	global_load_lds_dwordx4 v[126:127], off
	s_barrier
	s_waitcnt lgkmcnt(0)
	s_setprio 1
	s_waitcnt lgkmcnt(0)
	v_mfma_f32_16x16x32_f16 v[92:95], v[44:47], v[80:83], v[92:95]
	v_mfma_f32_16x16x32_f16 v[88:91], v[60:63], v[80:83], v[88:91]
	v_mfma_f32_16x16x32_f16 v[76:79], v[44:47], v[136:139], v[76:79]
	v_mfma_f32_16x16x32_f16 v[72:75], v[60:63], v[136:139], v[72:75]
	v_mfma_f32_16x16x32_f16 v[28:31], v[44:47], v[144:147], v[28:31]
	v_mfma_f32_16x16x32_f16 v[24:27], v[60:63], v[144:147], v[24:27]
	v_mfma_f32_16x16x32_f16 v[12:15], v[44:47], v[152:155], v[12:15]
	v_mfma_f32_16x16x32_f16 v[8:11], v[60:63], v[152:155], v[8:11]
	v_mfma_f32_16x16x32_f16 v[92:95], v[56:59], v[96:99], v[92:95]
	v_mfma_f32_16x16x32_f16 v[88:91], v[64:67], v[96:99], v[88:91]
	v_mfma_f32_16x16x32_f16 v[76:79], v[56:59], v[140:143], v[76:79]
	v_mfma_f32_16x16x32_f16 v[72:75], v[64:67], v[140:143], v[72:75]
	v_mfma_f32_16x16x32_f16 v[28:31], v[56:59], v[148:151], v[28:31]
	v_mfma_f32_16x16x32_f16 v[24:27], v[64:67], v[148:151], v[24:27]
	v_mfma_f32_16x16x32_f16 v[12:15], v[56:59], v[156:159], v[12:15]
	v_mfma_f32_16x16x32_f16 v[8:11], v[64:67], v[156:159], v[8:11]
	s_setprio 0
	s_barrier
	s_add_i32 s46, s48, s54
	v_lshl_add_u64 v[126:127], v[166:167], 0, s[22:23]
	s_mov_b32 m0, s46
	ds_read_b128 v[44:47], v134
	ds_read_b128 v[56:59], v134 offset:1024
	ds_read_b128 v[60:63], v134 offset:2048
	ds_read_b128 v[64:67], v134 offset:3072
	global_load_lds_dwordx4 v[126:127], off
	v_lshl_add_u64 v[126:127], v[168:169], 0, s[22:23]
	s_add_i32 m0, s46, 0x2000
	s_nop 0
	global_load_lds_dwordx4 v[126:127], off
	s_waitcnt vmcnt(6)
	s_barrier
	s_waitcnt lgkmcnt(0)
	s_setprio 1
	s_waitcnt lgkmcnt(0)
	v_mfma_f32_16x16x32_f16 v[84:87], v[44:47], v[80:83], v[84:87]
	v_mfma_f32_16x16x32_f16 v[68:71], v[60:63], v[80:83], v[68:71]
	v_mfma_f32_16x16x32_f16 v[52:55], v[44:47], v[136:139], v[52:55]
	v_mfma_f32_16x16x32_f16 v[48:51], v[60:63], v[136:139], v[48:51]
	v_mfma_f32_16x16x32_f16 v[20:23], v[44:47], v[144:147], v[20:23]
	v_mfma_f32_16x16x32_f16 v[16:19], v[60:63], v[144:147], v[16:19]
	v_mfma_f32_16x16x32_f16 v[4:7], v[44:47], v[152:155], v[4:7]
	v_mfma_f32_16x16x32_f16 v[0:3], v[60:63], v[152:155], v[0:3]
	v_mfma_f32_16x16x32_f16 v[84:87], v[56:59], v[96:99], v[84:87]
	v_mfma_f32_16x16x32_f16 v[80:83], v[64:67], v[96:99], v[68:71]
	v_mfma_f32_16x16x32_f16 v[52:55], v[56:59], v[140:143], v[52:55]
	v_mfma_f32_16x16x32_f16 v[48:51], v[64:67], v[140:143], v[48:51]
	v_mfma_f32_16x16x32_f16 v[20:23], v[56:59], v[148:151], v[20:23]
	v_mfma_f32_16x16x32_f16 v[16:19], v[64:67], v[148:151], v[16:19]
	v_mfma_f32_16x16x32_f16 v[4:7], v[56:59], v[156:159], v[4:7]
	v_mfma_f32_16x16x32_f16 v[0:3], v[64:67], v[156:159], v[0:3]
	s_setprio 0
	s_barrier
	s_add_i32 s75, s75, 3
	s_add_u32 s44, s44, 0x180
	s_addc_u32 s45, s45, 0
	s_branch .LBB5_42

	.amdhsa_kernel _Z9k_gemm128IN4g1289EpiGeluLNEEvNS0_4GemmET_
		.amdhsa_group_segment_fixed_size 0
		.amdhsa_private_segment_fixed_size 0
		.amdhsa_kernarg_size 344
		.amdhsa_user_sgpr_count 2
		.amdhsa_user_sgpr_dispatch_ptr 0
		.amdhsa_user_sgpr_queue_ptr 0
		.amdhsa_user_sgpr_kernarg_segment_ptr 1
		.amdhsa_user_sgpr_dispatch_id 0
		.amdhsa_user_sgpr_kernarg_preload_length 0
		.amdhsa_user_sgpr_kernarg_preload_offset 0
		.amdhsa_user_sgpr_private_segment_size 0
		.amdhsa_uses_dynamic_stack 0
		.amdhsa_enable_private_segment 0
		.amdhsa_system_sgpr_workgroup_id_x 1
		.amdhsa_system_sgpr_workgroup_id_y 0
		.amdhsa_system_sgpr_workgroup_id_z 0
		.amdhsa_system_sgpr_workgroup_info 0
		.amdhsa_system_vgpr_workitem_id 0
		.amdhsa_next_free_vgpr 256
		.amdhsa_next_free_sgpr 98
		.amdhsa_accum_offset 256
		.amdhsa_reserve_vcc 1
		.amdhsa_float_round_mode_32 0
		.amdhsa_float_round_mode_16_64 0
		.amdhsa_float_denorm_mode_32 3
		.amdhsa_float_denorm_mode_16_64 3
		.amdhsa_dx10_clamp 1
		.amdhsa_ieee_mode 1
		.amdhsa_fp16_overflow 0
		.amdhsa_tg_split 0
		.amdhsa_exception_fp_ieee_invalid_op 0
		.amdhsa_exception_fp_denorm_src 0
		.amdhsa_exception_fp_ieee_div_zero 0
		.amdhsa_exception_fp_ieee_overflow 0
		.amdhsa_exception_fp_ieee_underflow 0
		.amdhsa_exception_fp_ieee_inexact 0
		.amdhsa_exception_int_div_zero 0
	.end_amdhsa_kernel

amdhsa.kernels:
  - .agpr_count:     0
    .args:
      - .offset:         0
        .size:           224
        .value_kind:     by_value
      - .actual_access:  read_only
        .address_space:  global
        .offset:         224
        .size:           8
        .value_kind:     global_buffer
      - .actual_access:  read_only
        .address_space:  global
        .offset:         232
        .size:           8
        .value_kind:     global_buffer
      - .actual_access:  read_only
        .address_space:  global
        .offset:         240
        .size:           8
        .value_kind:     global_buffer
      - .actual_access:  write_only
        .address_space:  global
        .offset:         248
        .size:           8
        .value_kind:     global_buffer
      - .offset:         256
        .size:           4
        .value_kind:     hidden_block_count_x
      - .offset:         260
        .size:           4
        .value_kind:     hidden_block_count_y
      - .offset:         264
        .size:           4
        .value_kind:     hidden_block_count_z
      - .offset:         268
        .size:           2
        .value_kind:     hidden_group_size_x
      - .offset:         270
        .size:           2
        .value_kind:     hidden_group_size_y
      - .offset:         272
        .size:           2
        .value_kind:     hidden_group_size_z
      - .offset:         274
        .size:           2
        .value_kind:     hidden_remainder_x
      - .offset:         276
        .size:           2
        .value_kind:     hidden_remainder_y
      - .offset:         278
        .size:           2
        .value_kind:     hidden_remainder_z
      - .offset:         296
        .size:           8
        .value_kind:     hidden_global_offset_x
      - .offset:         304
        .size:           8
        .value_kind:     hidden_global_offset_y
      - .offset:         312
        .size:           8
        .value_kind:     hidden_global_offset_z
      - .offset:         320
        .size:           2
        .value_kind:     hidden_grid_dims
    .group_segment_fixed_size: 16640
    .kernarg_segment_align: 8
    .kernarg_segment_size: 512
    .language:       OpenCL C
    .language_version:
      - 2
      - 0
    .max_flat_workgroup_size: 256
    .name:           _Z10k_prep_ln18PrepArgsPKfS1_S1_Pt
    .private_segment_fixed_size: 0
    .sgpr_count:     28
    .sgpr_spill_count: 0
    .symbol:         _Z10k_prep_ln18PrepArgsPKfS1_S1_Pt.kd
    .uniform_work_group_size: 1
    .uses_dynamic_stack: false
    .vgpr_count:     75
    .vgpr_spill_count: 0
    .wavefront_size: 64
  - .agpr_count:     0
    .args:
      - .actual_access:  read_only
        .address_space:  global
        .offset:         0
        .size:           8
        .value_kind:     global_buffer
      - .actual_access:  read_only
        .address_space:  global
        .offset:         8
        .size:           8
        .value_kind:     global_buffer
      - .actual_access:  read_only
        .address_space:  global
        .offset:         16
        .size:           8
        .value_kind:     global_buffer
      - .actual_access:  write_only
        .address_space:  global
        .offset:         24
        .size:           8
        .value_kind:     global_buffer
    .group_segment_fixed_size: 0
    .kernarg_segment_align: 8
    .kernarg_segment_size: 32
    .language:       OpenCL C
    .language_version:
      - 2
      - 0
    .max_flat_workgroup_size: 256
    .name:           _Z5k_ln2PKfS0_S0_Pt
    .private_segment_fixed_size: 0
    .sgpr_count:     18
    .sgpr_spill_count: 0
    .symbol:         _Z5k_ln2PKfS0_S0_Pt.kd
    .uniform_work_group_size: 1
    .uses_dynamic_stack: false
    .vgpr_count:     54
    .vgpr_spill_count: 0
    .wavefront_size: 64
  - .agpr_count:     0
    .args:
      - .actual_access:  read_only
        .address_space:  global
        .offset:         0
        .size:           8
        .value_kind:     global_buffer
      - .actual_access:  read_only
        .address_space:  global
        .offset:         8
        .size:           8
        .value_kind:     global_buffer
      - .actual_access:  read_only
        .address_space:  global
        .offset:         16
        .size:           8
        .value_kind:     global_buffer
      - .actual_access:  read_only
        .address_space:  global
        .offset:         24
        .size:           8
        .value_kind:     global_buffer
      - .actual_access:  read_only
        .address_space:  global
        .offset:         32
        .size:           8
        .value_kind:     global_buffer
      - .actual_access:  write_only
        .address_space:  global
        .offset:         40
        .size:           8
        .value_kind:     global_buffer
      - .offset:         48
        .size:           224
        .value_kind:     by_value
    .group_segment_fixed_size: 0
    .kernarg_segment_align: 8
    .kernarg_segment_size: 272
    .language:       OpenCL C
    .language_version:
      - 2
      - 0
    .max_flat_workgroup_size: 256
    .name:           _Z6k_attnPKtS0_S0_S0_S0_Pt8PrepArgs
    .private_segment_fixed_size: 0
    .sgpr_count:     30
    .sgpr_spill_count: 0
    .symbol:         _Z6k_attnPKtS0_S0_S0_S0_Pt8PrepArgs.kd
    .uniform_work_group_size: 1
    .uses_dynamic_stack: false
    .vgpr_count:     244
    .vgpr_spill_count: 0
    .wavefront_size: 64
  - .agpr_count:     0
    .args:
      - .offset:         0
        .size:           40
        .value_kind:     by_value
      - .offset:         40
        .size:           32
        .value_kind:     by_value
      - .offset:         72
        .size:           4
        .value_kind:     hidden_block_count_x
      - .offset:         76
        .size:           4
        .value_kind:     hidden_block_count_y
      - .offset:         80
        .size:           4
        .value_kind:     hidden_block_count_z
      - .offset:         84
        .size:           2
        .value_kind:     hidden_group_size_x
      - .offset:         86
        .size:           2
        .value_kind:     hidden_group_size_y
      - .offset:         88
        .size:           2
        .value_kind:     hidden_group_size_z
      - .offset:         90
        .size:           2
        .value_kind:     hidden_remainder_x
      - .offset:         92
        .size:           2
        .value_kind:     hidden_remainder_y
      - .offset:         94
        .size:           2
        .value_kind:     hidden_remainder_z
      - .offset:         112
        .size:           8
        .value_kind:     hidden_global_offset_x
      - .offset:         120
        .size:           8
        .value_kind:     hidden_global_offset_y
      - .offset:         128
        .size:           8
        .value_kind:     hidden_global_offset_z
      - .offset:         136
        .size:           2
        .value_kind:     hidden_grid_dims
      - .offset:         192
        .size:           4
        .value_kind:     hidden_dynamic_lds_size
    .group_segment_fixed_size: 0
    .kernarg_segment_align: 8
    .kernarg_segment_size: 328
    .language:       OpenCL C
    .language_version:
      - 2
      - 0
    .max_flat_workgroup_size: 512
    .name:           _Z9k_gemm192IN4g1926EpiQKVEEvNS0_4GemmET_
    .private_segment_fixed_size: 0
    .sgpr_count:     74
    .sgpr_spill_count: 0
    .symbol:         _Z9k_gemm192IN4g1926EpiQKVEEvNS0_4GemmET_.kd
    .uniform_work_group_size: 1
    .uses_dynamic_stack: false
    .vgpr_count:     156
    .vgpr_spill_count: 0
    .wavefront_size: 64
  - .agpr_count:     0
    .args:
      - .offset:         0
        .size:           40
        .value_kind:     by_value
      - .offset:         40
        .size:           48
        .value_kind:     by_value
      - .offset:         88
        .size:           4
        .value_kind:     hidden_block_count_x
      - .offset:         92
        .size:           4
        .value_kind:     hidden_block_count_y
      - .offset:         96
        .size:           4
        .value_kind:     hidden_block_count_z
      - .offset:         100
        .size:           2
        .value_kind:     hidden_group_size_x
      - .offset:         102
        .size:           2
        .value_kind:     hidden_group_size_y
      - .offset:         104
        .size:           2
        .value_kind:     hidden_group_size_z
      - .offset:         106
        .size:           2
        .value_kind:     hidden_remainder_x
      - .offset:         108
        .size:           2
        .value_kind:     hidden_remainder_y
      - .offset:         110
        .size:           2
        .value_kind:     hidden_remainder_z
      - .offset:         128
        .size:           8
        .value_kind:     hidden_global_offset_x
      - .offset:         136
        .size:           8
        .value_kind:     hidden_global_offset_y
      - .offset:         144
        .size:           8
        .value_kind:     hidden_global_offset_z
      - .offset:         152
        .size:           2
        .value_kind:     hidden_grid_dims
      - .offset:         208
        .size:           4
        .value_kind:     hidden_dynamic_lds_size
    .group_segment_fixed_size: 0
    .kernarg_segment_align: 8
    .kernarg_segment_size: 344
    .language:       OpenCL C
    .language_version:
      - 2
      - 0
    .max_flat_workgroup_size: 512
    .name:           _Z9k_gemm192IN4g19210EpiResStatEEvNS0_4GemmET_
    .private_segment_fixed_size: 0
    .sgpr_count:     78
    .sgpr_spill_count: 0
    .symbol:         _Z9k_gemm192IN4g19210EpiResStatEEvNS0_4GemmET_.kd
    .uniform_work_group_size: 1
    .uses_dynamic_stack: false
    .vgpr_count:     216
    .vgpr_spill_count: 0
    .wavefront_size: 64
  - .agpr_count:     0
    .args:
      - .offset:         0
        .size:           40
        .value_kind:     by_value
      - .offset:         40
        .size:           48
        .value_kind:     by_value
      - .offset:         88
        .size:           4
        .value_kind:     hidden_block_count_x
      - .offset:         92
        .size:           4
        .value_kind:     hidden_block_count_y
      - .offset:         96
        .size:           4
        .value_kind:     hidden_block_count_z
      - .offset:         100
        .size:           2
        .value_kind:     hidden_group_size_x
      - .offset:         102
        .size:           2
        .value_kind:     hidden_group_size_y
      - .offset:         104
        .size:           2
        .value_kind:     hidden_group_size_z
      - .offset:         106
        .size:           2
        .value_kind:     hidden_remainder_x
      - .offset:         108
        .size:           2
        .value_kind:     hidden_remainder_y
      - .offset:         110
        .size:           2
        .value_kind:     hidden_remainder_z
      - .offset:         128
        .size:           8
        .value_kind:     hidden_global_offset_x
      - .offset:         136
        .size:           8
        .value_kind:     hidden_global_offset_y
      - .offset:         144
        .size:           8
        .value_kind:     hidden_global_offset_z
      - .offset:         152
        .size:           2
        .value_kind:     hidden_grid_dims
      - .offset:         208
        .size:           4
        .value_kind:     hidden_dynamic_lds_size
    .group_segment_fixed_size: 0
    .kernarg_segment_align: 8
    .kernarg_segment_size: 344
    .language:       OpenCL C
    .language_version:
      - 2
      - 0
    .max_flat_workgroup_size: 512
    .name:           _Z9k_gemm128IN4g1289EpiGeluLNEEvNS0_4GemmET_
    .private_segment_fixed_size: 0
    .sgpr_count:     84
    .sgpr_spill_count: 0
    .symbol:         _Z9k_gemm128IN4g1289EpiGeluLNEEvNS0_4GemmET_.kd
    .uniform_work_group_size: 1
    .uses_dynamic_stack: false
    .vgpr_count:     256
    .vgpr_spill_count: 0
    .wavefront_size: 64
  - .agpr_count:     0
    .args:
      - .offset:         0
        .size:           40
        .value_kind:     by_value
      - .offset:         40
        .size:           32
        .value_kind:     by_value
      - .offset:         72
        .size:           4
        .value_kind:     hidden_block_count_x
      - .offset:         76
        .size:           4
        .value_kind:     hidden_block_count_y
      - .offset:         80
        .size:           4
        .value_kind:     hidden_block_count_z
      - .offset:         84
        .size:           2
        .value_kind:     hidden_group_size_x
      - .offset:         86
        .size:           2
        .value_kind:     hidden_group_size_y
      - .offset:         88
        .size:           2
        .value_kind:     hidden_group_size_z
      - .offset:         90
        .size:           2
        .value_kind:     hidden_remainder_x
      - .offset:         92
        .size:           2
        .value_kind:     hidden_remainder_y
      - .offset:         94
        .size:           2
        .value_kind:     hidden_remainder_z
      - .offset:         112
        .size:           8
        .value_kind:     hidden_global_offset_x
      - .offset:         120
        .size:           8
        .value_kind:     hidden_global_offset_y
      - .offset:         128
        .size:           8
        .value_kind:     hidden_global_offset_z
      - .offset:         136
        .size:           2
        .value_kind:     hidden_grid_dims
      - .offset:         192
        .size:           4
        .value_kind:     hidden_dynamic_lds_size
    .group_segment_fixed_size: 0
    .kernarg_segment_align: 8
    .kernarg_segment_size: 328
    .language:       OpenCL C
    .language_version:
      - 2
      - 0
    .max_flat_workgroup_size: 512
    .name:           _Z9k_gemm192IN4g1927EpiResHEEvNS0_4GemmET_
    .private_segment_fixed_size: 0
    .sgpr_count:     76
    .sgpr_spill_count: 0
    .symbol:         _Z9k_gemm192IN4g1927EpiResHEEvNS0_4GemmET_.kd
    .uniform_work_group_size: 1
    .uses_dynamic_stack: false
    .vgpr_count:     190
    .vgpr_spill_count: 0
    .wavefront_size: 64
